# int8 GEMM epilogues (input projection, V^T, output projection, FFN down): the eight per-row scale loads of a tile issued together up front, per-group vmcnt(0) waits (which also waited for the previous
# speedup vs baseline: 1.0064x; 1.0000x over previous
.LBB0_556:
	s_lshl_b32 s5, s5, 8
	v_lshl_add_u32 v164, s4, 8, v187
	v_or_b32_e32 v27, s5, v189
	v_mul_lo_u32 v26, s65, v164
	v_add_u32_e32 v27, s44, v27
	v_add_lshl_u32 v168, v27, v26, 1
	v_add_u32_e32 v154, s5, v190
	v_mov_b32_e32 v165, v155
	v_cvt_f32_i32_e32 v143, v143
	v_lshl_add_u64 v[30:31], v[154:155], 2, s[24:25]
	v_lshl_add_u64 v[26:27], v[164:165], 2, s[36:37]
	global_load_dword v170, v[26:27], off
	global_load_dword v240, v[26:27], off offset:64
	global_load_dword v241, v[26:27], off offset:128
	global_load_dword v242, v[26:27], off offset:192
	global_load_dword v243, v[26:27], off offset:512
	global_load_dword v244, v[26:27], off offset:576
	global_load_dword v245, v[26:27], off offset:640
	global_load_dword v246, v[26:27], off offset:704
	global_load_dwordx4 v[46:49], v[30:31], off
	global_load_dwordx4 v[42:45], v[30:31], off offset:16
	s_nop 0
	global_load_dwordx4 v[26:29], v[30:31], off offset:528
	s_nop 0
	global_load_dwordx4 v[30:33], v[30:31], off offset:512
	v_cvt_f32_i32_e32 v142, v142
	v_cvt_f32_i32_e32 v139, v139
	v_cvt_f32_i32_e32 v138, v138
	v_cvt_f32_i32_e32 v145, v145
	v_cvt_f32_i32_e32 v144, v144
	v_cvt_f32_i32_e32 v141, v141
	v_cvt_f32_i32_e32 v140, v140
	s_xor_b64 s[34:35], s[34:35], -1
	v_cndmask_b32_e64 v154, 0, 1, s[42:43]
	s_mov_b64 s[44:45], -1
	s_and_b64 vcc, exec, s[34:35]
	v_cmp_ne_u32_e64 s[4:5], 1, v154
	s_waitcnt vmcnt(0)
	v_pk_mul_f32 v[194:195], v[46:47], v[170:171] op_sel_hi:[1,0]
	v_pk_mul_f32 v[196:197], v[42:43], v[170:171] op_sel_hi:[1,0]
	v_pk_mul_f32 v[198:199], v[48:49], v[170:171] op_sel_hi:[1,0]
	v_pk_mul_f32 v[200:201], v[44:45], v[170:171] op_sel_hi:[1,0]
	v_pk_mul_f32 v[142:143], v[194:195], v[142:143]
	v_pk_mul_f32 v[138:139], v[196:197], v[138:139]
	v_pk_mul_f32 v[144:145], v[198:199], v[144:145]
	v_pk_mul_f32 v[140:141], v[200:201], v[140:141]
	s_cbranch_vccz .LBB0_559
	s_and_b64 vcc, exec, s[4:5]
	s_cbranch_vccnz .LBB0_639
	v_mul_f32_e32 v154, 0xbfb8aa3b, v142
	v_exp_f32_e32 v154, v154
	v_mul_f32_e32 v165, 0xbfb8aa3b, v138
	v_exp_f32_e32 v165, v165
	v_mul_f32_e32 v169, 0xbfb8aa3b, v139
	v_add_f32_e32 v154, 1.0, v154
	v_rcp_f32_e32 v172, v154
	v_mul_f32_e32 v154, 0xbfb8aa3b, v143
	v_exp_f32_e32 v154, v154
	v_exp_f32_e32 v169, v169
	v_add_f32_e32 v165, 1.0, v165
	v_rcp_f32_e32 v176, v165
	v_add_f32_e32 v154, 1.0, v154
	v_mul_f32_e32 v165, 0xbfb8aa3b, v144
	v_rcp_f32_e32 v173, v154
	v_add_f32_e32 v154, 1.0, v169
	v_exp_f32_e32 v165, v165
	v_mul_f32_e32 v169, 0xbfb8aa3b, v140
	v_exp_f32_e32 v169, v169
	v_rcp_f32_e32 v177, v154
	v_add_f32_e32 v154, 1.0, v165
	v_mul_f32_e32 v165, 0xbfb8aa3b, v145
	v_rcp_f32_e32 v174, v154
	v_add_f32_e32 v154, 1.0, v169
	v_exp_f32_e32 v165, v165
	v_mul_f32_e32 v169, 0xbfb8aa3b, v141
	v_exp_f32_e32 v169, v169
	v_rcp_f32_e32 v178, v154
	v_add_f32_e32 v154, 1.0, v165
	v_rcp_f32_e32 v175, v154
	v_add_f32_e32 v154, 1.0, v169
	v_rcp_f32_e32 v179, v154
	s_mov_b64 s[44:45], 0

.LBB0_566:
	v_mov_b32_e32 v169, v155
	v_lshl_add_u64 v[134:135], s[88:89], 0, v[168:169]
	v_cvt_pk_f16_f32 v130, v138, v139
	v_cvt_pk_f16_f32 v131, v140, v141
	v_cvt_pk_f16_f32 v132, v142, v143
	v_cvt_pk_f16_f32 v133, v144, v145
	v_add_u32_e32 v154, 16, v164
	global_store_dwordx4 v[134:135], v[130:133], off offset:256
	v_cvt_f32_i32_e32 v127, v127
	v_cvt_f32_i32_e32 v126, v126
	v_lshl_add_u64 v[130:131], v[154:155], 2, s[36:37]
	s_nop 0
	v_mov_b32_e32 v130, v240
	v_cvt_f32_i32_e32 v123, v123
	v_cvt_f32_i32_e32 v122, v122
	v_cvt_f32_i32_e32 v129, v129
	v_cvt_f32_i32_e32 v128, v128
	v_cvt_f32_i32_e32 v125, v125
	v_cvt_f32_i32_e32 v124, v124
	s_and_b64 vcc, exec, s[6:7]
	s_mov_b64 s[34:35], -1
	v_pk_mul_f32 v[132:133], v[46:47], v[130:131] op_sel_hi:[1,0]
	v_pk_mul_f32 v[134:135], v[42:43], v[130:131] op_sel_hi:[1,0]
	v_pk_mul_f32 v[136:137], v[48:49], v[130:131] op_sel_hi:[1,0]
	v_pk_mul_f32 v[138:139], v[44:45], v[130:131] op_sel_hi:[1,0]
	v_pk_mul_f32 v[126:127], v[132:133], v[126:127]
	v_pk_mul_f32 v[122:123], v[134:135], v[122:123]
	v_pk_mul_f32 v[128:129], v[136:137], v[128:129]
	v_pk_mul_f32 v[124:125], v[138:139], v[124:125]
	s_cbranch_vccnz .LBB0_569
	s_and_b64 vcc, exec, s[4:5]
	s_cbranch_vccnz .LBB0_641
	v_mul_f32_e32 v131, 0xbfb8aa3b, v126
	v_exp_f32_e32 v131, v131
	v_mul_f32_e32 v132, 0xbfb8aa3b, v122
	v_exp_f32_e32 v132, v132
	v_mul_f32_e32 v134, 0xbfb8aa3b, v123
	v_add_f32_e32 v131, 1.0, v131
	v_exp_f32_e32 v134, v134
	v_add_f32_e32 v133, 1.0, v132
	v_rcp_f32_e32 v132, v131
	v_mul_f32_e32 v131, 0xbfb8aa3b, v127
	v_exp_f32_e32 v131, v131
	v_rcp_f32_e32 v136, v133
	v_mul_f32_e32 v135, 0xbfb8aa3b, v124
	v_exp_f32_e32 v135, v135
	v_add_f32_e32 v131, 1.0, v131
	v_rcp_f32_e32 v133, v131
	v_add_f32_e32 v131, 1.0, v134
	v_mul_f32_e32 v134, 0xbfb8aa3b, v128
	v_exp_f32_e32 v134, v134
	v_rcp_f32_e32 v137, v131
	v_mul_f32_e32 v138, 0xbfb8aa3b, v125
	v_exp_f32_e32 v139, v138
	v_add_f32_e32 v131, 1.0, v134
	v_rcp_f32_e32 v134, v131
	v_add_f32_e32 v131, 1.0, v135
	v_mul_f32_e32 v135, 0xbfb8aa3b, v129
	v_exp_f32_e32 v135, v135
	v_rcp_f32_e32 v138, v131
	s_mov_b64 s[34:35], 0
	v_add_f32_e32 v131, 1.0, v135
	v_rcp_f32_e32 v135, v131
	v_add_f32_e32 v131, 1.0, v139
	v_rcp_f32_e32 v139, v131

.LBB0_576:
	v_lshl_add_u64 v[118:119], s[88:89], 0, v[154:155]
	v_cvt_pk_f16_f32 v114, v122, v123
	v_cvt_pk_f16_f32 v115, v124, v125
	v_cvt_pk_f16_f32 v116, v126, v127
	v_cvt_pk_f16_f32 v117, v128, v129
	global_store_dwordx4 v[118:119], v[114:117], off offset:256
	v_cvt_f32_i32_e32 v111, v111
	v_cvt_f32_i32_e32 v110, v110
	v_add_u32_e32 v114, 32, v164
	v_mov_b32_e32 v115, v155
	v_lshl_add_u64 v[114:115], v[114:115], 2, s[36:37]
	s_nop 0
	v_mov_b32_e32 v114, v241
	v_cvt_f32_i32_e32 v107, v107
	v_cvt_f32_i32_e32 v106, v106
	v_cvt_f32_i32_e32 v113, v113
	v_cvt_f32_i32_e32 v112, v112
	v_cvt_f32_i32_e32 v109, v109
	v_cvt_f32_i32_e32 v108, v108
	s_and_b64 vcc, exec, s[6:7]
	s_mov_b64 s[34:35], -1
	v_pk_mul_f32 v[116:117], v[46:47], v[114:115] op_sel_hi:[1,0]
	v_pk_mul_f32 v[118:119], v[42:43], v[114:115] op_sel_hi:[1,0]
	v_pk_mul_f32 v[120:121], v[48:49], v[114:115] op_sel_hi:[1,0]
	v_pk_mul_f32 v[122:123], v[44:45], v[114:115] op_sel_hi:[1,0]
	v_pk_mul_f32 v[110:111], v[116:117], v[110:111]
	v_pk_mul_f32 v[106:107], v[118:119], v[106:107]
	v_pk_mul_f32 v[112:113], v[120:121], v[112:113]
	v_pk_mul_f32 v[108:109], v[122:123], v[108:109]
	s_cbranch_vccnz .LBB0_579
	s_and_b64 vcc, exec, s[4:5]
	s_cbranch_vccnz .LBB0_643
	v_mul_f32_e32 v115, 0xbfb8aa3b, v110
	v_exp_f32_e32 v115, v115
	v_mul_f32_e32 v116, 0xbfb8aa3b, v106
	v_exp_f32_e32 v116, v116
	v_mul_f32_e32 v118, 0xbfb8aa3b, v107
	v_add_f32_e32 v115, 1.0, v115
	v_exp_f32_e32 v118, v118
	v_add_f32_e32 v117, 1.0, v116
	v_rcp_f32_e32 v116, v115
	v_mul_f32_e32 v115, 0xbfb8aa3b, v111
	v_exp_f32_e32 v115, v115
	v_rcp_f32_e32 v120, v117
	v_mul_f32_e32 v119, 0xbfb8aa3b, v108
	v_exp_f32_e32 v119, v119
	v_add_f32_e32 v115, 1.0, v115
	v_rcp_f32_e32 v117, v115
	v_add_f32_e32 v115, 1.0, v118
	v_mul_f32_e32 v118, 0xbfb8aa3b, v112
	v_exp_f32_e32 v118, v118
	v_rcp_f32_e32 v121, v115
	v_mul_f32_e32 v122, 0xbfb8aa3b, v109
	v_exp_f32_e32 v123, v122
	v_add_f32_e32 v115, 1.0, v118
	v_rcp_f32_e32 v118, v115
	v_add_f32_e32 v115, 1.0, v119
	v_mul_f32_e32 v119, 0xbfb8aa3b, v113
	v_exp_f32_e32 v119, v119
	v_rcp_f32_e32 v122, v115
	s_mov_b64 s[34:35], 0
	v_add_f32_e32 v115, 1.0, v119
	v_rcp_f32_e32 v119, v115
	v_add_f32_e32 v115, 1.0, v123
	v_rcp_f32_e32 v123, v115

.LBB0_586:
	v_lshl_add_u64 v[102:103], s[88:89], 0, v[154:155]
	v_cvt_pk_f16_f32 v98, v106, v107
	v_cvt_pk_f16_f32 v99, v108, v109
	v_cvt_pk_f16_f32 v100, v110, v111
	v_cvt_pk_f16_f32 v101, v112, v113
	global_store_dwordx4 v[102:103], v[98:101], off offset:256
	v_cvt_f32_i32_e32 v95, v95
	v_cvt_f32_i32_e32 v94, v94
	v_add_u32_e32 v98, 48, v164
	v_mov_b32_e32 v99, v155
	v_lshl_add_u64 v[98:99], v[98:99], 2, s[36:37]
	s_nop 0
	v_mov_b32_e32 v98, v242
	v_cvt_f32_i32_e32 v91, v91
	v_cvt_f32_i32_e32 v90, v90
	v_cvt_f32_i32_e32 v97, v97
	v_cvt_f32_i32_e32 v96, v96
	v_cvt_f32_i32_e32 v93, v93
	v_cvt_f32_i32_e32 v92, v92
	s_and_b64 vcc, exec, s[6:7]
	s_mov_b64 s[34:35], -1
	v_pk_mul_f32 v[100:101], v[46:47], v[98:99] op_sel_hi:[1,0]
	v_pk_mul_f32 v[102:103], v[42:43], v[98:99] op_sel_hi:[1,0]
	v_pk_mul_f32 v[104:105], v[48:49], v[98:99] op_sel_hi:[1,0]
	v_pk_mul_f32 v[106:107], v[44:45], v[98:99] op_sel_hi:[1,0]
	v_pk_mul_f32 v[94:95], v[100:101], v[94:95]
	v_pk_mul_f32 v[90:91], v[102:103], v[90:91]
	v_pk_mul_f32 v[96:97], v[104:105], v[96:97]
	v_pk_mul_f32 v[92:93], v[106:107], v[92:93]
	s_cbranch_vccnz .LBB0_589
	s_and_b64 vcc, exec, s[4:5]
	s_cbranch_vccnz .LBB0_645
	v_mul_f32_e32 v99, 0xbfb8aa3b, v94
	v_exp_f32_e32 v99, v99
	v_mul_f32_e32 v100, 0xbfb8aa3b, v90
	v_exp_f32_e32 v100, v100
	v_mul_f32_e32 v102, 0xbfb8aa3b, v91
	v_add_f32_e32 v99, 1.0, v99
	v_exp_f32_e32 v102, v102
	v_add_f32_e32 v101, 1.0, v100
	v_rcp_f32_e32 v100, v99
	v_mul_f32_e32 v99, 0xbfb8aa3b, v95
	v_exp_f32_e32 v99, v99
	v_rcp_f32_e32 v104, v101
	v_mul_f32_e32 v103, 0xbfb8aa3b, v92
	v_exp_f32_e32 v103, v103
	v_add_f32_e32 v99, 1.0, v99
	v_rcp_f32_e32 v101, v99
	v_add_f32_e32 v99, 1.0, v102
	v_mul_f32_e32 v102, 0xbfb8aa3b, v96
	v_exp_f32_e32 v102, v102
	v_rcp_f32_e32 v105, v99
	v_mul_f32_e32 v106, 0xbfb8aa3b, v93
	v_exp_f32_e32 v107, v106
	v_add_f32_e32 v99, 1.0, v102
	v_rcp_f32_e32 v102, v99
	v_add_f32_e32 v99, 1.0, v103
	v_mul_f32_e32 v103, 0xbfb8aa3b, v97
	v_exp_f32_e32 v103, v103
	v_rcp_f32_e32 v106, v99
	s_mov_b64 s[34:35], 0
	v_add_f32_e32 v99, 1.0, v103
	v_rcp_f32_e32 v103, v99
	v_add_f32_e32 v99, 1.0, v107
	v_rcp_f32_e32 v107, v99

.LBB0_596:
	v_lshl_add_u64 v[86:87], s[88:89], 0, v[154:155]
	v_cvt_pk_f16_f32 v82, v90, v91
	v_cvt_pk_f16_f32 v83, v92, v93
	v_cvt_pk_f16_f32 v84, v94, v95
	v_cvt_pk_f16_f32 v85, v96, v97
	global_store_dwordx4 v[86:87], v[82:85], off offset:256
	v_cvt_f32_i32_e32 v79, v79
	v_cvt_f32_i32_e32 v78, v78
	v_add_u32_e32 v82, 0x80, v164
	v_mov_b32_e32 v83, v155
	v_lshl_add_u64 v[82:83], v[82:83], 2, s[36:37]
	s_nop 0
	v_mov_b32_e32 v82, v243
	v_cvt_f32_i32_e32 v75, v75
	v_cvt_f32_i32_e32 v74, v74
	v_cvt_f32_i32_e32 v81, v81
	v_cvt_f32_i32_e32 v80, v80
	v_cvt_f32_i32_e32 v77, v77
	v_cvt_f32_i32_e32 v76, v76
	s_and_b64 vcc, exec, s[6:7]
	s_mov_b64 s[34:35], -1
	v_pk_mul_f32 v[84:85], v[46:47], v[82:83] op_sel_hi:[1,0]
	v_pk_mul_f32 v[86:87], v[42:43], v[82:83] op_sel_hi:[1,0]
	v_pk_mul_f32 v[88:89], v[48:49], v[82:83] op_sel_hi:[1,0]
	v_pk_mul_f32 v[90:91], v[44:45], v[82:83] op_sel_hi:[1,0]
	v_pk_mul_f32 v[78:79], v[84:85], v[78:79]
	v_pk_mul_f32 v[74:75], v[86:87], v[74:75]
	v_pk_mul_f32 v[80:81], v[88:89], v[80:81]
	v_pk_mul_f32 v[76:77], v[90:91], v[76:77]
	s_cbranch_vccnz .LBB0_599
	s_and_b64 vcc, exec, s[4:5]
	s_cbranch_vccnz .LBB0_647
	v_mul_f32_e32 v83, 0xbfb8aa3b, v78
	v_exp_f32_e32 v83, v83
	v_mul_f32_e32 v84, 0xbfb8aa3b, v74
	v_exp_f32_e32 v84, v84
	v_mul_f32_e32 v86, 0xbfb8aa3b, v75
	v_add_f32_e32 v83, 1.0, v83
	v_exp_f32_e32 v86, v86
	v_add_f32_e32 v85, 1.0, v84
	v_rcp_f32_e32 v84, v83
	v_mul_f32_e32 v83, 0xbfb8aa3b, v79
	v_exp_f32_e32 v83, v83
	v_rcp_f32_e32 v88, v85
	v_mul_f32_e32 v87, 0xbfb8aa3b, v76
	v_exp_f32_e32 v87, v87
	v_add_f32_e32 v83, 1.0, v83
	v_rcp_f32_e32 v85, v83
	v_add_f32_e32 v83, 1.0, v86
	v_mul_f32_e32 v86, 0xbfb8aa3b, v80
	v_exp_f32_e32 v86, v86
	v_rcp_f32_e32 v89, v83
	v_mul_f32_e32 v90, 0xbfb8aa3b, v77
	v_exp_f32_e32 v91, v90
	v_add_f32_e32 v83, 1.0, v86
	v_rcp_f32_e32 v86, v83
	v_add_f32_e32 v83, 1.0, v87
	v_mul_f32_e32 v87, 0xbfb8aa3b, v81
	v_exp_f32_e32 v87, v87
	v_rcp_f32_e32 v90, v83
	s_mov_b64 s[34:35], 0
	v_add_f32_e32 v83, 1.0, v87
	v_rcp_f32_e32 v87, v83
	v_add_f32_e32 v83, 1.0, v91
	v_rcp_f32_e32 v91, v83

.LBB0_606:
	v_lshl_add_u64 v[70:71], s[88:89], 0, v[154:155]
	v_cvt_pk_f16_f32 v66, v74, v75
	v_cvt_pk_f16_f32 v67, v76, v77
	v_cvt_pk_f16_f32 v68, v78, v79
	v_cvt_pk_f16_f32 v69, v80, v81
	global_store_dwordx4 v[70:71], v[66:69], off offset:256
	v_cvt_f32_i32_e32 v63, v63
	v_cvt_f32_i32_e32 v62, v62
	v_add_u32_e32 v66, 0x90, v164
	v_mov_b32_e32 v67, v155
	v_lshl_add_u64 v[66:67], v[66:67], 2, s[36:37]
	s_nop 0
	v_mov_b32_e32 v66, v244
	v_cvt_f32_i32_e32 v59, v59
	v_cvt_f32_i32_e32 v58, v58
	v_cvt_f32_i32_e32 v65, v65
	v_cvt_f32_i32_e32 v64, v64
	v_cvt_f32_i32_e32 v61, v61
	v_cvt_f32_i32_e32 v60, v60
	s_and_b64 vcc, exec, s[6:7]
	s_mov_b64 s[34:35], -1
	v_pk_mul_f32 v[68:69], v[46:47], v[66:67] op_sel_hi:[1,0]
	v_pk_mul_f32 v[70:71], v[42:43], v[66:67] op_sel_hi:[1,0]
	v_pk_mul_f32 v[72:73], v[48:49], v[66:67] op_sel_hi:[1,0]
	v_pk_mul_f32 v[74:75], v[44:45], v[66:67] op_sel_hi:[1,0]
	v_pk_mul_f32 v[62:63], v[68:69], v[62:63]
	v_pk_mul_f32 v[58:59], v[70:71], v[58:59]
	v_pk_mul_f32 v[64:65], v[72:73], v[64:65]
	v_pk_mul_f32 v[60:61], v[74:75], v[60:61]
	s_cbranch_vccnz .LBB0_609
	s_and_b64 vcc, exec, s[4:5]
	s_cbranch_vccnz .LBB0_649
	v_mul_f32_e32 v67, 0xbfb8aa3b, v62
	v_exp_f32_e32 v67, v67
	v_mul_f32_e32 v68, 0xbfb8aa3b, v58
	v_exp_f32_e32 v68, v68
	v_mul_f32_e32 v70, 0xbfb8aa3b, v59
	v_add_f32_e32 v67, 1.0, v67
	v_exp_f32_e32 v70, v70
	v_add_f32_e32 v69, 1.0, v68
	v_rcp_f32_e32 v68, v67
	v_mul_f32_e32 v67, 0xbfb8aa3b, v63
	v_exp_f32_e32 v67, v67
	v_rcp_f32_e32 v72, v69
	v_mul_f32_e32 v71, 0xbfb8aa3b, v60
	v_exp_f32_e32 v71, v71
	v_add_f32_e32 v67, 1.0, v67
	v_rcp_f32_e32 v69, v67
	v_add_f32_e32 v67, 1.0, v70
	v_mul_f32_e32 v70, 0xbfb8aa3b, v64
	v_exp_f32_e32 v70, v70
	v_rcp_f32_e32 v73, v67
	v_mul_f32_e32 v74, 0xbfb8aa3b, v61
	v_exp_f32_e32 v75, v74
	v_add_f32_e32 v67, 1.0, v70
	v_rcp_f32_e32 v70, v67
	v_add_f32_e32 v67, 1.0, v71
	v_mul_f32_e32 v71, 0xbfb8aa3b, v65
	v_exp_f32_e32 v71, v71
	v_rcp_f32_e32 v74, v67
	s_mov_b64 s[34:35], 0
	v_add_f32_e32 v67, 1.0, v71
	v_rcp_f32_e32 v71, v67
	v_add_f32_e32 v67, 1.0, v75
	v_rcp_f32_e32 v75, v67

.LBB0_616:
	v_lshl_add_u64 v[54:55], s[88:89], 0, v[154:155]
	v_cvt_pk_f16_f32 v50, v58, v59
	v_cvt_pk_f16_f32 v51, v60, v61
	v_cvt_pk_f16_f32 v52, v62, v63
	v_cvt_pk_f16_f32 v53, v64, v65
	global_store_dwordx4 v[54:55], v[50:53], off offset:256
	v_cvt_f32_i32_e32 v39, v39
	v_cvt_f32_i32_e32 v38, v38
	v_add_u32_e32 v50, 0xa0, v164
	v_mov_b32_e32 v51, v155
	v_lshl_add_u64 v[50:51], v[50:51], 2, s[36:37]
	s_nop 0
	v_mov_b32_e32 v50, v245
	v_cvt_f32_i32_e32 v35, v35
	v_cvt_f32_i32_e32 v34, v34
	v_cvt_f32_i32_e32 v41, v41
	v_cvt_f32_i32_e32 v40, v40
	v_cvt_f32_i32_e32 v37, v37
	v_cvt_f32_i32_e32 v36, v36
	s_and_b64 vcc, exec, s[6:7]
	s_mov_b64 s[34:35], -1
	v_pk_mul_f32 v[52:53], v[46:47], v[50:51] op_sel_hi:[1,0]
	v_pk_mul_f32 v[54:55], v[42:43], v[50:51] op_sel_hi:[1,0]
	v_pk_mul_f32 v[56:57], v[48:49], v[50:51] op_sel_hi:[1,0]
	v_pk_mul_f32 v[58:59], v[44:45], v[50:51] op_sel_hi:[1,0]
	v_pk_mul_f32 v[38:39], v[52:53], v[38:39]
	v_pk_mul_f32 v[34:35], v[54:55], v[34:35]
	v_pk_mul_f32 v[40:41], v[56:57], v[40:41]
	v_pk_mul_f32 v[36:37], v[58:59], v[36:37]
	s_cbranch_vccnz .LBB0_619
	s_and_b64 vcc, exec, s[4:5]
	s_cbranch_vccnz .LBB0_651
	v_mul_f32_e32 v51, 0xbfb8aa3b, v38
	v_exp_f32_e32 v51, v51
	v_mul_f32_e32 v52, 0xbfb8aa3b, v34
	v_exp_f32_e32 v52, v52
	v_mul_f32_e32 v54, 0xbfb8aa3b, v35
	v_add_f32_e32 v51, 1.0, v51
	v_exp_f32_e32 v54, v54
	v_add_f32_e32 v53, 1.0, v52
	v_rcp_f32_e32 v52, v51
	v_mul_f32_e32 v51, 0xbfb8aa3b, v39
	v_exp_f32_e32 v51, v51
	v_rcp_f32_e32 v56, v53
	v_mul_f32_e32 v55, 0xbfb8aa3b, v36
	v_exp_f32_e32 v55, v55
	v_add_f32_e32 v51, 1.0, v51
	v_rcp_f32_e32 v53, v51
	v_add_f32_e32 v51, 1.0, v54
	v_mul_f32_e32 v54, 0xbfb8aa3b, v40
	v_exp_f32_e32 v54, v54
	v_rcp_f32_e32 v57, v51
	v_mul_f32_e32 v58, 0xbfb8aa3b, v37
	v_exp_f32_e32 v59, v58
	v_add_f32_e32 v51, 1.0, v54
	v_rcp_f32_e32 v54, v51
	v_add_f32_e32 v51, 1.0, v55
	v_mul_f32_e32 v55, 0xbfb8aa3b, v41
	v_exp_f32_e32 v55, v55
	v_rcp_f32_e32 v58, v51
	s_mov_b64 s[34:35], 0
	v_add_f32_e32 v51, 1.0, v55
	v_rcp_f32_e32 v55, v51
	v_add_f32_e32 v51, 1.0, v59
	v_rcp_f32_e32 v59, v51

.LBB0_626:
	v_lshl_add_u64 v[22:23], s[88:89], 0, v[154:155]
	v_cvt_pk_f16_f32 v18, v34, v35
	v_cvt_pk_f16_f32 v19, v36, v37
	v_cvt_pk_f16_f32 v20, v38, v39
	v_cvt_pk_f16_f32 v21, v40, v41
	global_store_dwordx4 v[22:23], v[18:21], off offset:256
	v_cvt_f32_i32_e32 v15, v15
	v_cvt_f32_i32_e32 v14, v14
	v_add_u32_e32 v18, 0xb0, v164
	v_mov_b32_e32 v19, v155
	v_lshl_add_u64 v[18:19], v[18:19], 2, s[36:37]
	s_nop 0
	v_mov_b32_e32 v18, v246
	v_cvt_f32_i32_e32 v11, v11
	v_cvt_f32_i32_e32 v10, v10
	v_cvt_f32_i32_e32 v17, v17
	v_cvt_f32_i32_e32 v16, v16
	v_cvt_f32_i32_e32 v13, v13
	v_cvt_f32_i32_e32 v12, v12
	s_and_b64 vcc, exec, s[6:7]
	s_mov_b64 s[34:35], -1
	v_pk_mul_f32 v[20:21], v[46:47], v[18:19] op_sel_hi:[1,0]
	v_pk_mul_f32 v[22:23], v[42:43], v[18:19] op_sel_hi:[1,0]
	v_pk_mul_f32 v[24:25], v[48:49], v[18:19] op_sel_hi:[1,0]
	v_pk_mul_f32 v[34:35], v[44:45], v[18:19] op_sel_hi:[1,0]
	v_pk_mul_f32 v[14:15], v[20:21], v[14:15]
	v_pk_mul_f32 v[10:11], v[22:23], v[10:11]
	v_pk_mul_f32 v[16:17], v[24:25], v[16:17]
	v_pk_mul_f32 v[12:13], v[34:35], v[12:13]
	s_cbranch_vccnz .LBB0_629
	s_and_b64 vcc, exec, s[4:5]
	s_cbranch_vccnz .LBB0_653
	v_mul_f32_e32 v19, 0xbfb8aa3b, v14
	v_exp_f32_e32 v19, v19
	v_mul_f32_e32 v20, 0xbfb8aa3b, v10
	v_exp_f32_e32 v20, v20
	v_mul_f32_e32 v22, 0xbfb8aa3b, v11
	v_add_f32_e32 v19, 1.0, v19
	v_exp_f32_e32 v22, v22
	v_add_f32_e32 v21, 1.0, v20
	v_rcp_f32_e32 v20, v19
	v_mul_f32_e32 v19, 0xbfb8aa3b, v15
	v_exp_f32_e32 v19, v19
	v_rcp_f32_e32 v24, v21
	v_mul_f32_e32 v23, 0xbfb8aa3b, v12
	v_exp_f32_e32 v23, v23
	v_add_f32_e32 v19, 1.0, v19
	v_rcp_f32_e32 v21, v19
	v_add_f32_e32 v19, 1.0, v22
	v_mul_f32_e32 v22, 0xbfb8aa3b, v16
	v_exp_f32_e32 v22, v22
	v_rcp_f32_e32 v25, v19
	v_mul_f32_e32 v34, 0xbfb8aa3b, v13
	v_exp_f32_e32 v35, v34
	v_add_f32_e32 v19, 1.0, v22
	v_rcp_f32_e32 v22, v19
	v_add_f32_e32 v19, 1.0, v23
	v_mul_f32_e32 v23, 0xbfb8aa3b, v17
	v_exp_f32_e32 v23, v23
	v_rcp_f32_e32 v34, v19
	s_mov_b64 s[34:35], 0
	v_add_f32_e32 v19, 1.0, v23
	v_rcp_f32_e32 v23, v19
	v_add_f32_e32 v19, 1.0, v35
	v_rcp_f32_e32 v35, v19

.LBB0_676:
	v_lshl_add_u32 v164, s34, 8, v168
	s_lshl_b32 s15, s72, 8
	v_lshl_add_u32 v122, v164, 14, s15
	v_or_b32_e32 v122, v122, v170
	v_lshlrev_b32_e32 v173, 1, v122
	v_or_b32_e32 v154, s15, v170
	v_mov_b32_e32 v165, v155
	v_cvt_f32_i32_e32 v143, v143
	v_lshl_add_u64 v[122:123], v[154:155], 2, s[10:11]
	v_lshl_add_u64 v[124:125], v[164:165], 2, s[12:13]
	global_load_dword v174, v[124:125], off
	global_load_dword v240, v[124:125], off offset:64
	global_load_dword v241, v[124:125], off offset:128
	global_load_dword v242, v[124:125], off offset:192
	global_load_dword v243, v[124:125], off offset:512
	global_load_dword v244, v[124:125], off offset:576
	global_load_dword v245, v[124:125], off offset:640
	global_load_dword v246, v[124:125], off offset:704
	global_load_dwordx4 v[134:137], v[122:123], off
	global_load_dwordx4 v[130:133], v[122:123], off offset:16
	global_load_dwordx4 v[126:129], v[122:123], off offset:512
	s_nop 0
	global_load_dwordx4 v[122:125], v[122:123], off offset:528
	v_cvt_f32_i32_e32 v142, v142
	v_cvt_f32_i32_e32 v145, v145
	v_cvt_f32_i32_e32 v144, v144
	v_cvt_f32_i32_e32 v139, v139
	v_cvt_f32_i32_e32 v138, v138
	v_cvt_f32_i32_e32 v141, v141
	v_cvt_f32_i32_e32 v140, v140
	v_cvt_f32_i32_e32 v119, v119
	v_cvt_f32_i32_e32 v118, v118
	v_cvt_f32_i32_e32 v121, v121
	v_cvt_f32_i32_e32 v120, v120
	v_cvt_f32_i32_e32 v115, v115
	v_cvt_f32_i32_e32 v114, v114
	v_cvt_f32_i32_e32 v117, v117
	v_cvt_f32_i32_e32 v116, v116
	v_add_u32_e32 v154, 16, v164
	v_lshl_add_u64 v[176:177], v[154:155], 2, s[12:13]
	v_cvt_f32_i32_e32 v111, v111
	v_cvt_f32_i32_e32 v110, v110
	v_cvt_f32_i32_e32 v113, v113
	v_cvt_f32_i32_e32 v112, v112
	v_cvt_f32_i32_e32 v107, v107
	v_cvt_f32_i32_e32 v106, v106
	v_cvt_f32_i32_e32 v109, v109
	v_cvt_f32_i32_e32 v108, v108
	v_cvt_f32_i32_e32 v103, v103
	v_cvt_f32_i32_e32 v102, v102
	v_cvt_f32_i32_e32 v105, v105
	v_cvt_f32_i32_e32 v104, v104
	v_cvt_f32_i32_e32 v99, v99
	v_cvt_f32_i32_e32 v98, v98
	v_cvt_f32_i32_e32 v101, v101
	v_cvt_f32_i32_e32 v100, v100
	v_add_u32_e32 v165, 0x80000, v173
	v_add_u32_e32 v154, 32, v164
	v_cvt_f32_i32_e32 v95, v95
	v_cvt_f32_i32_e32 v94, v94
	v_cvt_f32_i32_e32 v97, v97
	v_cvt_f32_i32_e32 v96, v96
	v_cvt_f32_i32_e32 v91, v91
	v_cvt_f32_i32_e32 v90, v90
	v_cvt_f32_i32_e32 v93, v93
	v_cvt_f32_i32_e32 v92, v92
	v_cvt_f32_i32_e32 v87, v87
	v_cvt_f32_i32_e32 v86, v86
	v_cvt_f32_i32_e32 v89, v89
	v_cvt_f32_i32_e32 v88, v88
	v_cvt_f32_i32_e32 v83, v83
	v_cvt_f32_i32_e32 v82, v82
	v_cvt_f32_i32_e32 v85, v85
	v_cvt_f32_i32_e32 v84, v84
	v_cvt_f32_i32_e32 v79, v79
	v_cvt_f32_i32_e32 v78, v78
	v_cvt_f32_i32_e32 v81, v81
	v_cvt_f32_i32_e32 v80, v80
	v_cvt_f32_i32_e32 v75, v75
	v_cvt_f32_i32_e32 v74, v74
	v_cvt_f32_i32_e32 v77, v77
	v_cvt_f32_i32_e32 v76, v76
	v_cvt_f32_i32_e32 v71, v71
	v_cvt_f32_i32_e32 v70, v70
	v_cvt_f32_i32_e32 v73, v73
	v_cvt_f32_i32_e32 v72, v72
	v_cvt_f32_i32_e32 v67, v67
	v_cvt_f32_i32_e32 v66, v66
	v_cvt_f32_i32_e32 v69, v69
	v_cvt_f32_i32_e32 v68, v68
	v_cvt_f32_i32_e32 v63, v63
	v_cvt_f32_i32_e32 v62, v62
	v_cvt_f32_i32_e32 v65, v65
	v_cvt_f32_i32_e32 v64, v64
	v_cvt_f32_i32_e32 v59, v59
	v_cvt_f32_i32_e32 v58, v58
	v_cvt_f32_i32_e32 v61, v61
	v_cvt_f32_i32_e32 v60, v60
	v_cvt_f32_i32_e32 v55, v55
	s_waitcnt vmcnt(0)
	v_pk_mul_f32 v[178:179], v[134:135], v[174:175] op_sel_hi:[1,0]
	v_pk_mul_f32 v[180:181], v[136:137], v[174:175] op_sel_hi:[1,0]
	v_pk_mul_f32 v[182:183], v[130:131], v[174:175] op_sel_hi:[1,0]
	v_pk_mul_f32 v[184:185], v[132:133], v[174:175] op_sel_hi:[1,0]
	v_pk_mul_f32 v[186:187], v[126:127], v[174:175] op_sel_hi:[1,0]
	v_pk_mul_f32 v[188:189], v[128:129], v[174:175] op_sel_hi:[1,0]
	v_pk_mul_f32 v[190:191], v[174:175], v[122:123] op_sel_hi:[0,1]
	v_pk_mul_f32 v[174:175], v[174:175], v[124:125] op_sel_hi:[0,1]
	v_pk_mul_f32 v[142:143], v[178:179], v[142:143]
	v_pk_mul_f32 v[144:145], v[180:181], v[144:145]
	v_pk_mul_f32 v[138:139], v[182:183], v[138:139]
	v_pk_mul_f32 v[140:141], v[184:185], v[140:141]
	v_pk_mul_f32 v[118:119], v[186:187], v[118:119]
	v_pk_mul_f32 v[120:121], v[188:189], v[120:121]
	v_pk_mul_f32 v[178:179], v[190:191], v[114:115]
	v_pk_mul_f32 v[174:175], v[174:175], v[116:117]
	v_cvt_pk_f16_f32 v114, v142, v143
	v_cvt_pk_f16_f32 v115, v144, v145
	v_cvt_pk_f16_f32 v116, v138, v139
	v_cvt_pk_f16_f32 v117, v140, v141
	v_cvt_pk_f16_f32 v118, v118, v119
	v_cvt_pk_f16_f32 v119, v120, v121
	v_cvt_pk_f16_f32 v120, v178, v179
	v_cvt_pk_f16_f32 v121, v174, v175
	global_store_dwordx4 v173, v[114:117], s[94:95]
	global_store_dwordx4 v173, v[118:121], s[94:95] offset:256
	s_nop 0
	v_mov_b32_e32 v114, v240
	v_lshl_add_u64 v[116:117], v[154:155], 2, s[12:13]
	v_add_u32_e32 v154, 48, v164
	v_cvt_f32_i32_e32 v54, v54
	v_cvt_f32_i32_e32 v57, v57
	v_cvt_f32_i32_e32 v56, v56
	v_cvt_f32_i32_e32 v51, v51
	v_cvt_f32_i32_e32 v50, v50
	v_cvt_f32_i32_e32 v53, v53
	v_cvt_f32_i32_e32 v52, v52
	v_cvt_f32_i32_e32 v47, v47
	v_cvt_f32_i32_e32 v46, v46
	v_cvt_f32_i32_e32 v49, v49
	v_cvt_f32_i32_e32 v48, v48
	v_cvt_f32_i32_e32 v43, v43
	v_cvt_f32_i32_e32 v42, v42
	v_cvt_f32_i32_e32 v45, v45
	v_cvt_f32_i32_e32 v44, v44
	v_cvt_f32_i32_e32 v39, v39
	v_cvt_f32_i32_e32 v38, v38
	v_cvt_f32_i32_e32 v41, v41
	v_cvt_f32_i32_e32 v40, v40
	v_cvt_f32_i32_e32 v35, v35
	v_cvt_f32_i32_e32 v34, v34
	v_cvt_f32_i32_e32 v37, v37
	v_cvt_f32_i32_e32 v36, v36
	v_cvt_f32_i32_e32 v31, v31
	v_cvt_f32_i32_e32 v30, v30
	v_cvt_f32_i32_e32 v33, v33
	v_cvt_f32_i32_e32 v32, v32
	v_cvt_f32_i32_e32 v27, v27
	v_cvt_f32_i32_e32 v26, v26
	v_cvt_f32_i32_e32 v29, v29
	v_cvt_f32_i32_e32 v28, v28
	v_cvt_f32_i32_e32 v23, v23
	v_cvt_f32_i32_e32 v22, v22
	v_cvt_f32_i32_e32 v25, v25
	v_cvt_f32_i32_e32 v24, v24
	v_cvt_f32_i32_e32 v19, v19
	v_cvt_f32_i32_e32 v18, v18
	v_cvt_f32_i32_e32 v21, v21
	v_cvt_f32_i32_e32 v20, v20
	v_cvt_f32_i32_e32 v15, v15
	v_cvt_f32_i32_e32 v14, v14
	v_cvt_f32_i32_e32 v17, v17
	v_cvt_f32_i32_e32 v16, v16
	v_cvt_f32_i32_e32 v11, v11
	v_cvt_f32_i32_e32 v10, v10
	v_cvt_f32_i32_e32 v13, v13
	v_cvt_f32_i32_e32 v12, v12
	v_cvt_f32_i32_e32 v7, v7
	v_cvt_f32_i32_e32 v6, v6
	v_cvt_f32_i32_e32 v9, v9
	v_cvt_f32_i32_e32 v8, v8
	v_cvt_f32_i32_e32 v3, v3
	v_cvt_f32_i32_e32 v2, v2
	v_cvt_f32_i32_e32 v5, v5
	v_cvt_f32_i32_e32 v4, v4
	s_andn2_b64 vcc, exec, s[2:3]
	s_mov_b64 s[2:3], -1
	v_pk_mul_f32 v[118:119], v[134:135], v[114:115] op_sel_hi:[1,0]
	v_pk_mul_f32 v[120:121], v[136:137], v[114:115] op_sel_hi:[1,0]
	v_pk_mul_f32 v[138:139], v[130:131], v[114:115] op_sel_hi:[1,0]
	v_pk_mul_f32 v[140:141], v[132:133], v[114:115] op_sel_hi:[1,0]
	v_pk_mul_f32 v[142:143], v[126:127], v[114:115] op_sel_hi:[1,0]
	v_pk_mul_f32 v[144:145], v[128:129], v[114:115] op_sel_hi:[1,0]
	v_pk_mul_f32 v[174:175], v[122:123], v[114:115] op_sel_hi:[1,0]
	v_pk_mul_f32 v[114:115], v[124:125], v[114:115] op_sel_hi:[1,0]
	v_pk_mul_f32 v[110:111], v[118:119], v[110:111]
	v_pk_mul_f32 v[112:113], v[120:121], v[112:113]
	v_pk_mul_f32 v[106:107], v[138:139], v[106:107]
	v_pk_mul_f32 v[108:109], v[140:141], v[108:109]
	v_pk_mul_f32 v[102:103], v[142:143], v[102:103]
	v_pk_mul_f32 v[104:105], v[144:145], v[104:105]
	v_pk_mul_f32 v[118:119], v[174:175], v[98:99]
	v_pk_mul_f32 v[114:115], v[114:115], v[100:101]
	v_cvt_pk_f16_f32 v98, v110, v111
	v_cvt_pk_f16_f32 v99, v112, v113
	v_cvt_pk_f16_f32 v100, v106, v107
	v_cvt_pk_f16_f32 v101, v108, v109
	v_cvt_pk_f16_f32 v102, v102, v103
	v_cvt_pk_f16_f32 v103, v104, v105
	v_cvt_pk_f16_f32 v104, v118, v119
	v_cvt_pk_f16_f32 v105, v114, v115
	global_store_dwordx4 v165, v[98:101], s[94:95]
	global_store_dwordx4 v165, v[102:105], s[94:95] offset:256
	s_nop 0
	v_mov_b32_e32 v98, v241
	v_add_u32_e32 v116, 0x100000, v173
	v_lshl_add_u64 v[100:101], v[154:155], 2, s[12:13]
	v_add_u32_e32 v154, 0x80, v164
	v_pk_mul_f32 v[102:103], v[134:135], v[98:99] op_sel_hi:[1,0]
	v_pk_mul_f32 v[104:105], v[136:137], v[98:99] op_sel_hi:[1,0]
	v_pk_mul_f32 v[106:107], v[130:131], v[98:99] op_sel_hi:[1,0]
	v_pk_mul_f32 v[108:109], v[132:133], v[98:99] op_sel_hi:[1,0]
	v_pk_mul_f32 v[110:111], v[126:127], v[98:99] op_sel_hi:[1,0]
	v_pk_mul_f32 v[112:113], v[128:129], v[98:99] op_sel_hi:[1,0]
	v_pk_mul_f32 v[114:115], v[122:123], v[98:99] op_sel_hi:[1,0]
	v_pk_mul_f32 v[98:99], v[124:125], v[98:99] op_sel_hi:[1,0]
	v_pk_mul_f32 v[94:95], v[102:103], v[94:95]
	v_pk_mul_f32 v[96:97], v[104:105], v[96:97]
	v_pk_mul_f32 v[90:91], v[106:107], v[90:91]
	v_pk_mul_f32 v[92:93], v[108:109], v[92:93]
	v_pk_mul_f32 v[86:87], v[110:111], v[86:87]
	v_pk_mul_f32 v[88:89], v[112:113], v[88:89]
	v_pk_mul_f32 v[102:103], v[114:115], v[82:83]
	v_pk_mul_f32 v[98:99], v[98:99], v[84:85]
	v_cvt_pk_f16_f32 v82, v94, v95
	v_cvt_pk_f16_f32 v83, v96, v97
	v_cvt_pk_f16_f32 v84, v90, v91
	v_cvt_pk_f16_f32 v85, v92, v93
	v_cvt_pk_f16_f32 v86, v86, v87
	v_cvt_pk_f16_f32 v87, v88, v89
	v_cvt_pk_f16_f32 v88, v102, v103
	v_cvt_pk_f16_f32 v89, v98, v99
	global_store_dwordx4 v116, v[82:85], s[94:95]
	global_store_dwordx4 v116, v[86:89], s[94:95] offset:256
	s_nop 0
	v_mov_b32_e32 v82, v242
	v_add_u32_e32 v100, 0x180000, v173
	v_lshl_add_u64 v[84:85], v[154:155], 2, s[12:13]
	v_add_u32_e32 v154, 0x90, v164
	v_pk_mul_f32 v[86:87], v[134:135], v[82:83] op_sel_hi:[1,0]
	v_pk_mul_f32 v[88:89], v[136:137], v[82:83] op_sel_hi:[1,0]
	v_pk_mul_f32 v[90:91], v[130:131], v[82:83] op_sel_hi:[1,0]
	v_pk_mul_f32 v[92:93], v[132:133], v[82:83] op_sel_hi:[1,0]
	v_pk_mul_f32 v[94:95], v[126:127], v[82:83] op_sel_hi:[1,0]
	v_pk_mul_f32 v[96:97], v[128:129], v[82:83] op_sel_hi:[1,0]
	v_pk_mul_f32 v[98:99], v[122:123], v[82:83] op_sel_hi:[1,0]
	v_pk_mul_f32 v[82:83], v[124:125], v[82:83] op_sel_hi:[1,0]
	v_pk_mul_f32 v[78:79], v[86:87], v[78:79]
	v_pk_mul_f32 v[80:81], v[88:89], v[80:81]
	v_pk_mul_f32 v[74:75], v[90:91], v[74:75]
	v_pk_mul_f32 v[76:77], v[92:93], v[76:77]
	v_pk_mul_f32 v[70:71], v[94:95], v[70:71]
	v_pk_mul_f32 v[72:73], v[96:97], v[72:73]
	v_pk_mul_f32 v[86:87], v[98:99], v[66:67]
	v_pk_mul_f32 v[82:83], v[82:83], v[68:69]
	v_cvt_pk_f16_f32 v66, v78, v79
	v_cvt_pk_f16_f32 v67, v80, v81
	v_cvt_pk_f16_f32 v68, v74, v75
	v_cvt_pk_f16_f32 v69, v76, v77
	v_cvt_pk_f16_f32 v70, v70, v71
	v_cvt_pk_f16_f32 v71, v72, v73
	v_cvt_pk_f16_f32 v72, v86, v87
	v_cvt_pk_f16_f32 v73, v82, v83
	global_store_dwordx4 v100, v[66:69], s[94:95]
	global_store_dwordx4 v100, v[70:73], s[94:95] offset:256
	s_nop 0
	v_mov_b32_e32 v66, v243
	v_add_u32_e32 v84, 0x400000, v173
	v_lshl_add_u64 v[68:69], v[154:155], 2, s[12:13]
	v_add_u32_e32 v154, 0xa0, v164
	v_pk_mul_f32 v[70:71], v[134:135], v[66:67] op_sel_hi:[1,0]
	v_pk_mul_f32 v[72:73], v[136:137], v[66:67] op_sel_hi:[1,0]
	v_pk_mul_f32 v[74:75], v[130:131], v[66:67] op_sel_hi:[1,0]
	v_pk_mul_f32 v[76:77], v[132:133], v[66:67] op_sel_hi:[1,0]
	v_pk_mul_f32 v[78:79], v[126:127], v[66:67] op_sel_hi:[1,0]
	v_pk_mul_f32 v[80:81], v[128:129], v[66:67] op_sel_hi:[1,0]
	v_pk_mul_f32 v[82:83], v[122:123], v[66:67] op_sel_hi:[1,0]
	v_pk_mul_f32 v[66:67], v[124:125], v[66:67] op_sel_hi:[1,0]
	v_pk_mul_f32 v[62:63], v[70:71], v[62:63]
	v_pk_mul_f32 v[64:65], v[72:73], v[64:65]
	v_pk_mul_f32 v[58:59], v[74:75], v[58:59]
	v_pk_mul_f32 v[60:61], v[76:77], v[60:61]
	v_pk_mul_f32 v[54:55], v[78:79], v[54:55]
	v_pk_mul_f32 v[56:57], v[80:81], v[56:57]
	v_pk_mul_f32 v[70:71], v[82:83], v[50:51]
	v_pk_mul_f32 v[66:67], v[66:67], v[52:53]
	v_cvt_pk_f16_f32 v50, v62, v63
	v_cvt_pk_f16_f32 v51, v64, v65
	v_cvt_pk_f16_f32 v52, v58, v59
	v_cvt_pk_f16_f32 v53, v60, v61
	v_cvt_pk_f16_f32 v54, v54, v55
	v_cvt_pk_f16_f32 v55, v56, v57
	v_cvt_pk_f16_f32 v56, v70, v71
	v_cvt_pk_f16_f32 v57, v66, v67
	global_store_dwordx4 v84, v[50:53], s[94:95]
	global_store_dwordx4 v84, v[54:57], s[94:95] offset:256
	s_nop 0
	v_mov_b32_e32 v50, v244
	v_add_u32_e32 v68, 0x480000, v173
	v_lshl_add_u64 v[52:53], v[154:155], 2, s[12:13]
	v_add_u32_e32 v154, 0xb0, v164
	v_pk_mul_f32 v[54:55], v[134:135], v[50:51] op_sel_hi:[1,0]
	v_pk_mul_f32 v[56:57], v[136:137], v[50:51] op_sel_hi:[1,0]
	v_pk_mul_f32 v[58:59], v[130:131], v[50:51] op_sel_hi:[1,0]
	v_pk_mul_f32 v[60:61], v[132:133], v[50:51] op_sel_hi:[1,0]
	v_pk_mul_f32 v[62:63], v[126:127], v[50:51] op_sel_hi:[1,0]
	v_pk_mul_f32 v[64:65], v[128:129], v[50:51] op_sel_hi:[1,0]
	v_pk_mul_f32 v[66:67], v[122:123], v[50:51] op_sel_hi:[1,0]
	v_pk_mul_f32 v[50:51], v[124:125], v[50:51] op_sel_hi:[1,0]
	v_pk_mul_f32 v[46:47], v[54:55], v[46:47]
	v_pk_mul_f32 v[48:49], v[56:57], v[48:49]
	v_pk_mul_f32 v[42:43], v[58:59], v[42:43]
	v_pk_mul_f32 v[44:45], v[60:61], v[44:45]
	v_pk_mul_f32 v[38:39], v[62:63], v[38:39]
	v_pk_mul_f32 v[40:41], v[64:65], v[40:41]
	v_pk_mul_f32 v[54:55], v[66:67], v[34:35]
	v_pk_mul_f32 v[50:51], v[50:51], v[36:37]
	v_cvt_pk_f16_f32 v34, v46, v47
	v_cvt_pk_f16_f32 v35, v48, v49
	v_cvt_pk_f16_f32 v36, v42, v43
	v_cvt_pk_f16_f32 v37, v44, v45
	v_cvt_pk_f16_f32 v38, v38, v39
	v_cvt_pk_f16_f32 v39, v40, v41
	v_cvt_pk_f16_f32 v40, v54, v55
	v_cvt_pk_f16_f32 v41, v50, v51
	global_store_dwordx4 v68, v[34:37], s[94:95]
	global_store_dwordx4 v68, v[38:41], s[94:95] offset:256
	s_nop 0
	v_mov_b32_e32 v34, v245
	v_add_u32_e32 v52, 0x500000, v173
	v_lshl_add_u64 v[36:37], v[154:155], 2, s[12:13]
	v_pk_mul_f32 v[38:39], v[134:135], v[34:35] op_sel_hi:[1,0]
	v_pk_mul_f32 v[40:41], v[136:137], v[34:35] op_sel_hi:[1,0]
	v_pk_mul_f32 v[42:43], v[130:131], v[34:35] op_sel_hi:[1,0]
	v_pk_mul_f32 v[44:45], v[132:133], v[34:35] op_sel_hi:[1,0]
	v_pk_mul_f32 v[46:47], v[126:127], v[34:35] op_sel_hi:[1,0]
	v_pk_mul_f32 v[48:49], v[128:129], v[34:35] op_sel_hi:[1,0]
	v_pk_mul_f32 v[50:51], v[122:123], v[34:35] op_sel_hi:[1,0]
	v_pk_mul_f32 v[34:35], v[124:125], v[34:35] op_sel_hi:[1,0]
	v_pk_mul_f32 v[30:31], v[38:39], v[30:31]
	v_pk_mul_f32 v[32:33], v[40:41], v[32:33]
	v_pk_mul_f32 v[26:27], v[42:43], v[26:27]
	v_pk_mul_f32 v[28:29], v[44:45], v[28:29]
	v_pk_mul_f32 v[22:23], v[46:47], v[22:23]
	v_pk_mul_f32 v[24:25], v[48:49], v[24:25]
	v_pk_mul_f32 v[38:39], v[50:51], v[18:19]
	v_pk_mul_f32 v[34:35], v[34:35], v[20:21]
	v_cvt_pk_f16_f32 v18, v30, v31
	v_cvt_pk_f16_f32 v19, v32, v33
	v_cvt_pk_f16_f32 v20, v26, v27
	v_cvt_pk_f16_f32 v21, v28, v29
	v_cvt_pk_f16_f32 v22, v22, v23
	v_cvt_pk_f16_f32 v23, v24, v25
	v_cvt_pk_f16_f32 v24, v38, v39
	v_cvt_pk_f16_f32 v25, v34, v35
	global_store_dwordx4 v52, v[18:21], s[94:95]
	global_store_dwordx4 v52, v[22:25], s[94:95] offset:256
	s_nop 0
	v_mov_b32_e32 v18, v246
	v_add_u32_e32 v34, 0x580000, v173
	v_pk_mul_f32 v[20:21], v[134:135], v[18:19] op_sel_hi:[1,0]
	v_pk_mul_f32 v[22:23], v[136:137], v[18:19] op_sel_hi:[1,0]
	v_pk_mul_f32 v[24:25], v[130:131], v[18:19] op_sel_hi:[1,0]
	v_pk_mul_f32 v[26:27], v[132:133], v[18:19] op_sel_hi:[1,0]
	v_pk_mul_f32 v[28:29], v[126:127], v[18:19] op_sel_hi:[1,0]
	v_pk_mul_f32 v[30:31], v[128:129], v[18:19] op_sel_hi:[1,0]
	v_pk_mul_f32 v[32:33], v[122:123], v[18:19] op_sel_hi:[1,0]
	v_pk_mul_f32 v[18:19], v[124:125], v[18:19] op_sel_hi:[1,0]
	v_pk_mul_f32 v[14:15], v[20:21], v[14:15]
	v_pk_mul_f32 v[16:17], v[22:23], v[16:17]
	v_pk_mul_f32 v[10:11], v[24:25], v[10:11]
	v_pk_mul_f32 v[12:13], v[26:27], v[12:13]
	v_pk_mul_f32 v[6:7], v[28:29], v[6:7]
	v_pk_mul_f32 v[8:9], v[30:31], v[8:9]
	v_pk_mul_f32 v[20:21], v[32:33], v[2:3]
	v_pk_mul_f32 v[18:19], v[18:19], v[4:5]
	v_cvt_pk_f16_f32 v2, v14, v15
	v_cvt_pk_f16_f32 v3, v16, v17
	v_cvt_pk_f16_f32 v4, v10, v11
	v_cvt_pk_f16_f32 v5, v12, v13
	v_cvt_pk_f16_f32 v6, v6, v7
	v_cvt_pk_f16_f32 v7, v8, v9
	v_cvt_pk_f16_f32 v8, v20, v21
	v_cvt_pk_f16_f32 v9, v18, v19
	global_store_dwordx4 v34, v[2:5], s[94:95]
	global_store_dwordx4 v34, v[6:9], s[94:95] offset:256
	s_cbranch_vccnz .LBB0_665
	s_andn2_b64 vcc, exec, s[4:5]
	s_cbranch_vccnz .LBB0_664
	s_barrier
	s_branch .LBB0_664

.LBB0_1492:
	v_lshl_or_b32 v154, s48, 8, v168
	v_lshl_add_u32 v164, s22, 8, v1
	v_lshlrev_b32_e32 v122, 1, v154
	v_lshl_add_u32 v172, v164, 13, v122
	v_mov_b32_e32 v165, v155
	v_cvt_f32_i32_e32 v143, v143
	v_lshl_add_u64 v[122:123], v[154:155], 2, s[8:9]
	v_lshl_add_u64 v[124:125], v[164:165], 2, s[6:7]
	global_load_dword v174, v[124:125], off
	global_load_dword v240, v[124:125], off offset:64
	global_load_dword v241, v[124:125], off offset:128
	global_load_dword v242, v[124:125], off offset:192
	global_load_dword v243, v[124:125], off offset:512
	global_load_dword v244, v[124:125], off offset:576
	global_load_dword v245, v[124:125], off offset:640
	global_load_dword v246, v[124:125], off offset:704
	global_load_dwordx4 v[134:137], v[122:123], off
	global_load_dwordx4 v[130:133], v[122:123], off offset:16
	global_load_dwordx4 v[126:129], v[122:123], off offset:512
	s_nop 0
	global_load_dwordx4 v[122:125], v[122:123], off offset:528
	v_cvt_f32_i32_e32 v142, v142
	v_cvt_f32_i32_e32 v145, v145
	v_cvt_f32_i32_e32 v144, v144
	v_cvt_f32_i32_e32 v139, v139
	v_cvt_f32_i32_e32 v138, v138
	v_cvt_f32_i32_e32 v141, v141
	v_cvt_f32_i32_e32 v140, v140
	v_cvt_f32_i32_e32 v119, v119
	v_cvt_f32_i32_e32 v118, v118
	v_cvt_f32_i32_e32 v121, v121
	v_cvt_f32_i32_e32 v120, v120
	v_cvt_f32_i32_e32 v115, v115
	v_cvt_f32_i32_e32 v114, v114
	v_cvt_f32_i32_e32 v117, v117
	v_cvt_f32_i32_e32 v116, v116
	v_add_u32_e32 v154, 16, v164
	v_lshl_add_u64 v[176:177], v[154:155], 2, s[6:7]
	v_cvt_f32_i32_e32 v111, v111
	v_cvt_f32_i32_e32 v110, v110
	v_cvt_f32_i32_e32 v113, v113
	v_cvt_f32_i32_e32 v112, v112
	v_cvt_f32_i32_e32 v107, v107
	v_cvt_f32_i32_e32 v106, v106
	v_cvt_f32_i32_e32 v109, v109
	v_cvt_f32_i32_e32 v108, v108
	v_cvt_f32_i32_e32 v103, v103
	v_cvt_f32_i32_e32 v102, v102
	v_cvt_f32_i32_e32 v105, v105
	v_cvt_f32_i32_e32 v104, v104
	v_cvt_f32_i32_e32 v99, v99
	v_cvt_f32_i32_e32 v98, v98
	v_cvt_f32_i32_e32 v101, v101
	v_cvt_f32_i32_e32 v100, v100
	v_add_u32_e32 v165, 0x20000, v172
	v_add_u32_e32 v154, 32, v164
	v_cvt_f32_i32_e32 v95, v95
	v_cvt_f32_i32_e32 v94, v94
	v_cvt_f32_i32_e32 v97, v97
	v_cvt_f32_i32_e32 v96, v96
	v_cvt_f32_i32_e32 v91, v91
	v_cvt_f32_i32_e32 v90, v90
	v_cvt_f32_i32_e32 v93, v93
	v_cvt_f32_i32_e32 v92, v92
	v_cvt_f32_i32_e32 v87, v87
	v_cvt_f32_i32_e32 v86, v86
	v_cvt_f32_i32_e32 v89, v89
	v_cvt_f32_i32_e32 v88, v88
	v_cvt_f32_i32_e32 v83, v83
	v_cvt_f32_i32_e32 v82, v82
	v_cvt_f32_i32_e32 v85, v85
	v_cvt_f32_i32_e32 v84, v84
	v_cvt_f32_i32_e32 v79, v79
	v_cvt_f32_i32_e32 v78, v78
	v_cvt_f32_i32_e32 v81, v81
	v_cvt_f32_i32_e32 v80, v80
	v_cvt_f32_i32_e32 v75, v75
	v_cvt_f32_i32_e32 v74, v74
	v_cvt_f32_i32_e32 v77, v77
	v_cvt_f32_i32_e32 v76, v76
	v_cvt_f32_i32_e32 v71, v71
	v_cvt_f32_i32_e32 v70, v70
	v_cvt_f32_i32_e32 v73, v73
	v_cvt_f32_i32_e32 v72, v72
	v_cvt_f32_i32_e32 v67, v67
	v_cvt_f32_i32_e32 v66, v66
	v_cvt_f32_i32_e32 v69, v69
	v_cvt_f32_i32_e32 v68, v68
	v_cvt_f32_i32_e32 v63, v63
	v_cvt_f32_i32_e32 v62, v62
	v_cvt_f32_i32_e32 v65, v65
	v_cvt_f32_i32_e32 v64, v64
	v_cvt_f32_i32_e32 v59, v59
	v_cvt_f32_i32_e32 v58, v58
	v_cvt_f32_i32_e32 v61, v61
	v_cvt_f32_i32_e32 v60, v60
	v_cvt_f32_i32_e32 v55, v55
	s_waitcnt vmcnt(0)
	v_pk_mul_f32 v[178:179], v[134:135], v[174:175] op_sel_hi:[1,0]
	v_pk_mul_f32 v[180:181], v[136:137], v[174:175] op_sel_hi:[1,0]
	v_pk_mul_f32 v[182:183], v[130:131], v[174:175] op_sel_hi:[1,0]
	v_pk_mul_f32 v[184:185], v[132:133], v[174:175] op_sel_hi:[1,0]
	v_pk_mul_f32 v[186:187], v[126:127], v[174:175] op_sel_hi:[1,0]
	v_pk_mul_f32 v[188:189], v[128:129], v[174:175] op_sel_hi:[1,0]
	v_pk_mul_f32 v[190:191], v[122:123], v[174:175] op_sel_hi:[1,0]
	v_pk_mul_f32 v[174:175], v[124:125], v[174:175] op_sel_hi:[1,0]
	v_pk_mul_f32 v[142:143], v[178:179], v[142:143]
	v_pk_mul_f32 v[144:145], v[180:181], v[144:145]
	v_pk_mul_f32 v[138:139], v[182:183], v[138:139]
	v_pk_mul_f32 v[140:141], v[184:185], v[140:141]
	v_pk_mul_f32 v[118:119], v[186:187], v[118:119]
	v_pk_mul_f32 v[120:121], v[188:189], v[120:121]
	v_pk_mul_f32 v[178:179], v[190:191], v[114:115]
	v_pk_mul_f32 v[174:175], v[174:175], v[116:117]
	v_cvt_pk_f16_f32 v114, v142, v143
	v_cvt_pk_f16_f32 v115, v144, v145
	v_cvt_pk_f16_f32 v116, v138, v139
	v_cvt_pk_f16_f32 v117, v140, v141
	v_cvt_pk_f16_f32 v118, v118, v119
	v_cvt_pk_f16_f32 v119, v120, v121
	v_cvt_pk_f16_f32 v120, v178, v179
	v_cvt_pk_f16_f32 v121, v174, v175
	global_store_dwordx4 v172, v[114:117], s[40:41]
	global_store_dwordx4 v172, v[118:121], s[40:41] offset:256
	s_nop 0
	v_mov_b32_e32 v114, v240
	v_lshl_add_u64 v[116:117], v[154:155], 2, s[6:7]
	v_add_u32_e32 v154, 48, v164
	v_cvt_f32_i32_e32 v54, v54
	v_cvt_f32_i32_e32 v57, v57
	v_cvt_f32_i32_e32 v56, v56
	v_cvt_f32_i32_e32 v51, v51
	v_cvt_f32_i32_e32 v50, v50
	v_cvt_f32_i32_e32 v53, v53
	v_cvt_f32_i32_e32 v52, v52
	v_cvt_f32_i32_e32 v47, v47
	v_cvt_f32_i32_e32 v46, v46
	v_cvt_f32_i32_e32 v49, v49
	v_cvt_f32_i32_e32 v48, v48
	v_cvt_f32_i32_e32 v43, v43
	v_cvt_f32_i32_e32 v42, v42
	v_cvt_f32_i32_e32 v45, v45
	v_cvt_f32_i32_e32 v44, v44
	v_cvt_f32_i32_e32 v39, v39
	v_cvt_f32_i32_e32 v38, v38
	v_cvt_f32_i32_e32 v41, v41
	v_cvt_f32_i32_e32 v40, v40
	v_cvt_f32_i32_e32 v35, v35
	v_cvt_f32_i32_e32 v34, v34
	v_cvt_f32_i32_e32 v37, v37
	v_cvt_f32_i32_e32 v36, v36
	v_cvt_f32_i32_e32 v31, v31
	v_cvt_f32_i32_e32 v30, v30
	v_cvt_f32_i32_e32 v33, v33
	v_cvt_f32_i32_e32 v32, v32
	v_cvt_f32_i32_e32 v27, v27
	v_cvt_f32_i32_e32 v26, v26
	v_cvt_f32_i32_e32 v29, v29
	v_cvt_f32_i32_e32 v28, v28
	v_cvt_f32_i32_e32 v23, v23
	v_cvt_f32_i32_e32 v22, v22
	v_cvt_f32_i32_e32 v25, v25
	v_cvt_f32_i32_e32 v24, v24
	v_cvt_f32_i32_e32 v19, v19
	v_cvt_f32_i32_e32 v18, v18
	v_cvt_f32_i32_e32 v21, v21
	v_cvt_f32_i32_e32 v20, v20
	v_cvt_f32_i32_e32 v15, v15
	v_cvt_f32_i32_e32 v14, v14
	v_cvt_f32_i32_e32 v17, v17
	v_cvt_f32_i32_e32 v16, v16
	v_cvt_f32_i32_e32 v11, v11
	v_cvt_f32_i32_e32 v10, v10
	v_cvt_f32_i32_e32 v13, v13
	v_cvt_f32_i32_e32 v12, v12
	v_cvt_f32_i32_e32 v7, v7
	v_cvt_f32_i32_e32 v6, v6
	v_cvt_f32_i32_e32 v9, v9
	v_cvt_f32_i32_e32 v8, v8
	v_cvt_f32_i32_e32 v3, v3
	v_cvt_f32_i32_e32 v2, v2
	v_cvt_f32_i32_e32 v5, v5
	v_cvt_f32_i32_e32 v4, v4
	s_andn2_b64 vcc, exec, s[2:3]
	s_mov_b64 s[2:3], -1
	v_pk_mul_f32 v[118:119], v[134:135], v[114:115] op_sel_hi:[1,0]
	v_pk_mul_f32 v[120:121], v[136:137], v[114:115] op_sel_hi:[1,0]
	v_pk_mul_f32 v[138:139], v[130:131], v[114:115] op_sel_hi:[1,0]
	v_pk_mul_f32 v[140:141], v[132:133], v[114:115] op_sel_hi:[1,0]
	v_pk_mul_f32 v[142:143], v[126:127], v[114:115] op_sel_hi:[1,0]
	v_pk_mul_f32 v[144:145], v[128:129], v[114:115] op_sel_hi:[1,0]
	v_pk_mul_f32 v[174:175], v[122:123], v[114:115] op_sel_hi:[1,0]
	v_pk_mul_f32 v[114:115], v[124:125], v[114:115] op_sel_hi:[1,0]
	v_pk_mul_f32 v[110:111], v[118:119], v[110:111]
	v_pk_mul_f32 v[112:113], v[120:121], v[112:113]
	v_pk_mul_f32 v[106:107], v[138:139], v[106:107]
	v_pk_mul_f32 v[108:109], v[140:141], v[108:109]
	v_pk_mul_f32 v[102:103], v[142:143], v[102:103]
	v_pk_mul_f32 v[104:105], v[144:145], v[104:105]
	v_pk_mul_f32 v[118:119], v[174:175], v[98:99]
	v_pk_mul_f32 v[114:115], v[114:115], v[100:101]
	v_cvt_pk_f16_f32 v98, v110, v111
	v_cvt_pk_f16_f32 v99, v112, v113
	v_cvt_pk_f16_f32 v100, v106, v107
	v_cvt_pk_f16_f32 v101, v108, v109
	v_cvt_pk_f16_f32 v102, v102, v103
	v_cvt_pk_f16_f32 v103, v104, v105
	v_cvt_pk_f16_f32 v104, v118, v119
	v_cvt_pk_f16_f32 v105, v114, v115
	global_store_dwordx4 v165, v[98:101], s[40:41]
	global_store_dwordx4 v165, v[102:105], s[40:41] offset:256
	s_nop 0
	v_mov_b32_e32 v98, v241
	v_add_u32_e32 v116, 0x40000, v172
	v_lshl_add_u64 v[100:101], v[154:155], 2, s[6:7]
	v_add_u32_e32 v154, 0x80, v164
	v_pk_mul_f32 v[102:103], v[134:135], v[98:99] op_sel_hi:[1,0]
	v_pk_mul_f32 v[104:105], v[136:137], v[98:99] op_sel_hi:[1,0]
	v_pk_mul_f32 v[106:107], v[130:131], v[98:99] op_sel_hi:[1,0]
	v_pk_mul_f32 v[108:109], v[132:133], v[98:99] op_sel_hi:[1,0]
	v_pk_mul_f32 v[110:111], v[126:127], v[98:99] op_sel_hi:[1,0]
	v_pk_mul_f32 v[112:113], v[128:129], v[98:99] op_sel_hi:[1,0]
	v_pk_mul_f32 v[114:115], v[122:123], v[98:99] op_sel_hi:[1,0]
	v_pk_mul_f32 v[98:99], v[124:125], v[98:99] op_sel_hi:[1,0]
	v_pk_mul_f32 v[94:95], v[102:103], v[94:95]
	v_pk_mul_f32 v[96:97], v[104:105], v[96:97]
	v_pk_mul_f32 v[90:91], v[106:107], v[90:91]
	v_pk_mul_f32 v[92:93], v[108:109], v[92:93]
	v_pk_mul_f32 v[86:87], v[110:111], v[86:87]
	v_pk_mul_f32 v[88:89], v[112:113], v[88:89]
	v_pk_mul_f32 v[102:103], v[114:115], v[82:83]
	v_pk_mul_f32 v[98:99], v[98:99], v[84:85]
	v_cvt_pk_f16_f32 v82, v94, v95
	v_cvt_pk_f16_f32 v83, v96, v97
	v_cvt_pk_f16_f32 v84, v90, v91
	v_cvt_pk_f16_f32 v85, v92, v93
	v_cvt_pk_f16_f32 v86, v86, v87
	v_cvt_pk_f16_f32 v87, v88, v89
	v_cvt_pk_f16_f32 v88, v102, v103
	v_cvt_pk_f16_f32 v89, v98, v99
	global_store_dwordx4 v116, v[82:85], s[40:41]
	global_store_dwordx4 v116, v[86:89], s[40:41] offset:256
	s_nop 0
	v_mov_b32_e32 v82, v242
	v_add_u32_e32 v100, 0x60000, v172
	v_lshl_add_u64 v[84:85], v[154:155], 2, s[6:7]
	v_add_u32_e32 v154, 0x90, v164
	v_pk_mul_f32 v[86:87], v[134:135], v[82:83] op_sel_hi:[1,0]
	v_pk_mul_f32 v[88:89], v[136:137], v[82:83] op_sel_hi:[1,0]
	v_pk_mul_f32 v[90:91], v[130:131], v[82:83] op_sel_hi:[1,0]
	v_pk_mul_f32 v[92:93], v[132:133], v[82:83] op_sel_hi:[1,0]
	v_pk_mul_f32 v[94:95], v[126:127], v[82:83] op_sel_hi:[1,0]
	v_pk_mul_f32 v[96:97], v[128:129], v[82:83] op_sel_hi:[1,0]
	v_pk_mul_f32 v[98:99], v[122:123], v[82:83] op_sel_hi:[1,0]
	v_pk_mul_f32 v[82:83], v[124:125], v[82:83] op_sel_hi:[1,0]
	v_pk_mul_f32 v[78:79], v[86:87], v[78:79]
	v_pk_mul_f32 v[80:81], v[88:89], v[80:81]
	v_pk_mul_f32 v[74:75], v[90:91], v[74:75]
	v_pk_mul_f32 v[76:77], v[92:93], v[76:77]
	v_pk_mul_f32 v[70:71], v[94:95], v[70:71]
	v_pk_mul_f32 v[72:73], v[96:97], v[72:73]
	v_pk_mul_f32 v[86:87], v[98:99], v[66:67]
	v_pk_mul_f32 v[82:83], v[82:83], v[68:69]
	v_cvt_pk_f16_f32 v66, v78, v79
	v_cvt_pk_f16_f32 v67, v80, v81
	v_cvt_pk_f16_f32 v68, v74, v75
	v_cvt_pk_f16_f32 v69, v76, v77
	v_cvt_pk_f16_f32 v70, v70, v71
	v_cvt_pk_f16_f32 v71, v72, v73
	v_cvt_pk_f16_f32 v72, v86, v87
	v_cvt_pk_f16_f32 v73, v82, v83
	global_store_dwordx4 v100, v[66:69], s[40:41]
	global_store_dwordx4 v100, v[70:73], s[40:41] offset:256
	s_nop 0
	v_mov_b32_e32 v66, v243
	v_add_u32_e32 v84, 0x100000, v172
	v_lshl_add_u64 v[68:69], v[154:155], 2, s[6:7]
	v_add_u32_e32 v154, 0xa0, v164
	v_pk_mul_f32 v[70:71], v[134:135], v[66:67] op_sel_hi:[1,0]
	v_pk_mul_f32 v[72:73], v[136:137], v[66:67] op_sel_hi:[1,0]
	v_pk_mul_f32 v[74:75], v[130:131], v[66:67] op_sel_hi:[1,0]
	v_pk_mul_f32 v[76:77], v[132:133], v[66:67] op_sel_hi:[1,0]
	v_pk_mul_f32 v[78:79], v[126:127], v[66:67] op_sel_hi:[1,0]
	v_pk_mul_f32 v[80:81], v[128:129], v[66:67] op_sel_hi:[1,0]
	v_pk_mul_f32 v[82:83], v[122:123], v[66:67] op_sel_hi:[1,0]
	v_pk_mul_f32 v[66:67], v[124:125], v[66:67] op_sel_hi:[1,0]
	v_pk_mul_f32 v[62:63], v[70:71], v[62:63]
	v_pk_mul_f32 v[64:65], v[72:73], v[64:65]
	v_pk_mul_f32 v[58:59], v[74:75], v[58:59]
	v_pk_mul_f32 v[60:61], v[76:77], v[60:61]
	v_pk_mul_f32 v[54:55], v[78:79], v[54:55]
	v_pk_mul_f32 v[56:57], v[80:81], v[56:57]
	v_pk_mul_f32 v[70:71], v[82:83], v[50:51]
	v_pk_mul_f32 v[66:67], v[66:67], v[52:53]
	v_cvt_pk_f16_f32 v50, v62, v63
	v_cvt_pk_f16_f32 v51, v64, v65
	v_cvt_pk_f16_f32 v52, v58, v59
	v_cvt_pk_f16_f32 v53, v60, v61
	v_cvt_pk_f16_f32 v54, v54, v55
	v_cvt_pk_f16_f32 v55, v56, v57
	v_cvt_pk_f16_f32 v56, v70, v71
	v_cvt_pk_f16_f32 v57, v66, v67
	global_store_dwordx4 v84, v[50:53], s[40:41]
	global_store_dwordx4 v84, v[54:57], s[40:41] offset:256
	s_nop 0
	v_mov_b32_e32 v50, v244
	v_add_u32_e32 v68, 0x120000, v172
	v_lshl_add_u64 v[52:53], v[154:155], 2, s[6:7]
	v_add_u32_e32 v154, 0xb0, v164
	v_pk_mul_f32 v[54:55], v[134:135], v[50:51] op_sel_hi:[1,0]
	v_pk_mul_f32 v[56:57], v[136:137], v[50:51] op_sel_hi:[1,0]
	v_pk_mul_f32 v[58:59], v[130:131], v[50:51] op_sel_hi:[1,0]
	v_pk_mul_f32 v[60:61], v[132:133], v[50:51] op_sel_hi:[1,0]
	v_pk_mul_f32 v[62:63], v[126:127], v[50:51] op_sel_hi:[1,0]
	v_pk_mul_f32 v[64:65], v[128:129], v[50:51] op_sel_hi:[1,0]
	v_pk_mul_f32 v[66:67], v[122:123], v[50:51] op_sel_hi:[1,0]
	v_pk_mul_f32 v[50:51], v[124:125], v[50:51] op_sel_hi:[1,0]
	v_pk_mul_f32 v[46:47], v[54:55], v[46:47]
	v_pk_mul_f32 v[48:49], v[56:57], v[48:49]
	v_pk_mul_f32 v[42:43], v[58:59], v[42:43]
	v_pk_mul_f32 v[44:45], v[60:61], v[44:45]
	v_pk_mul_f32 v[38:39], v[62:63], v[38:39]
	v_pk_mul_f32 v[40:41], v[64:65], v[40:41]
	v_pk_mul_f32 v[54:55], v[66:67], v[34:35]
	v_pk_mul_f32 v[50:51], v[50:51], v[36:37]
	v_cvt_pk_f16_f32 v34, v46, v47
	v_cvt_pk_f16_f32 v35, v48, v49
	v_cvt_pk_f16_f32 v36, v42, v43
	v_cvt_pk_f16_f32 v37, v44, v45
	v_cvt_pk_f16_f32 v38, v38, v39
	v_cvt_pk_f16_f32 v39, v40, v41
	v_cvt_pk_f16_f32 v40, v54, v55
	v_cvt_pk_f16_f32 v41, v50, v51
	global_store_dwordx4 v68, v[34:37], s[40:41]
	global_store_dwordx4 v68, v[38:41], s[40:41] offset:256
	s_nop 0
	v_mov_b32_e32 v34, v245
	v_add_u32_e32 v52, 0x140000, v172
	v_lshl_add_u64 v[36:37], v[154:155], 2, s[6:7]
	v_pk_mul_f32 v[38:39], v[134:135], v[34:35] op_sel_hi:[1,0]
	v_pk_mul_f32 v[40:41], v[136:137], v[34:35] op_sel_hi:[1,0]
	v_pk_mul_f32 v[42:43], v[130:131], v[34:35] op_sel_hi:[1,0]
	v_pk_mul_f32 v[44:45], v[132:133], v[34:35] op_sel_hi:[1,0]
	v_pk_mul_f32 v[46:47], v[126:127], v[34:35] op_sel_hi:[1,0]
	v_pk_mul_f32 v[48:49], v[128:129], v[34:35] op_sel_hi:[1,0]
	v_pk_mul_f32 v[50:51], v[122:123], v[34:35] op_sel_hi:[1,0]
	v_pk_mul_f32 v[34:35], v[124:125], v[34:35] op_sel_hi:[1,0]
	v_pk_mul_f32 v[30:31], v[38:39], v[30:31]
	v_pk_mul_f32 v[32:33], v[40:41], v[32:33]
	v_pk_mul_f32 v[26:27], v[42:43], v[26:27]
	v_pk_mul_f32 v[28:29], v[44:45], v[28:29]
	v_pk_mul_f32 v[22:23], v[46:47], v[22:23]
	v_pk_mul_f32 v[24:25], v[48:49], v[24:25]
	v_pk_mul_f32 v[38:39], v[50:51], v[18:19]
	v_pk_mul_f32 v[34:35], v[34:35], v[20:21]
	v_cvt_pk_f16_f32 v18, v30, v31
	v_cvt_pk_f16_f32 v19, v32, v33
	v_cvt_pk_f16_f32 v20, v26, v27
	v_cvt_pk_f16_f32 v21, v28, v29
	v_cvt_pk_f16_f32 v22, v22, v23
	v_cvt_pk_f16_f32 v23, v24, v25
	v_cvt_pk_f16_f32 v24, v38, v39
	v_cvt_pk_f16_f32 v25, v34, v35
	global_store_dwordx4 v52, v[18:21], s[40:41]
	global_store_dwordx4 v52, v[22:25], s[40:41] offset:256
	s_nop 0
	v_mov_b32_e32 v18, v246
	v_add_u32_e32 v34, 0x160000, v172
	v_pk_mul_f32 v[20:21], v[134:135], v[18:19] op_sel_hi:[1,0]
	v_pk_mul_f32 v[22:23], v[136:137], v[18:19] op_sel_hi:[1,0]
	v_pk_mul_f32 v[24:25], v[130:131], v[18:19] op_sel_hi:[1,0]
	v_pk_mul_f32 v[26:27], v[132:133], v[18:19] op_sel_hi:[1,0]
	v_pk_mul_f32 v[28:29], v[126:127], v[18:19] op_sel_hi:[1,0]
	v_pk_mul_f32 v[30:31], v[128:129], v[18:19] op_sel_hi:[1,0]
	v_pk_mul_f32 v[32:33], v[122:123], v[18:19] op_sel_hi:[1,0]
	v_pk_mul_f32 v[18:19], v[124:125], v[18:19] op_sel_hi:[1,0]
	v_pk_mul_f32 v[14:15], v[20:21], v[14:15]
	v_pk_mul_f32 v[16:17], v[22:23], v[16:17]
	v_pk_mul_f32 v[10:11], v[24:25], v[10:11]
	v_pk_mul_f32 v[12:13], v[26:27], v[12:13]
	v_pk_mul_f32 v[6:7], v[28:29], v[6:7]
	v_pk_mul_f32 v[8:9], v[30:31], v[8:9]
	v_pk_mul_f32 v[20:21], v[32:33], v[2:3]
	v_pk_mul_f32 v[18:19], v[18:19], v[4:5]
	v_cvt_pk_f16_f32 v2, v14, v15
	v_cvt_pk_f16_f32 v3, v16, v17
	v_cvt_pk_f16_f32 v4, v10, v11
	v_cvt_pk_f16_f32 v5, v12, v13
	v_cvt_pk_f16_f32 v6, v6, v7
	v_cvt_pk_f16_f32 v7, v8, v9
	v_cvt_pk_f16_f32 v8, v20, v21
	v_cvt_pk_f16_f32 v9, v18, v19
	global_store_dwordx4 v34, v[2:5], s[40:41]
	global_store_dwordx4 v34, v[6:9], s[40:41] offset:256
	s_cbranch_vccnz .LBB0_1481
	s_andn2_b64 vcc, exec, s[4:5]
	s_cbranch_vccnz .LBB0_1480
	s_barrier
	s_branch .LBB0_1480

.LBB0_1902:
	v_lshl_or_b32 v154, s46, 8, v168
	v_lshl_add_u32 v164, s45, 8, v1
	v_lshlrev_b32_e32 v122, 1, v154
	v_lshl_add_u32 v172, v164, 13, v122
	v_mov_b32_e32 v165, v155
	v_cvt_f32_i32_e32 v143, v143
	v_lshl_add_u64 v[122:123], v[154:155], 2, s[10:11]
	v_lshl_add_u64 v[124:125], v[164:165], 2, s[8:9]
	global_load_dword v174, v[124:125], off
	global_load_dword v240, v[124:125], off offset:64
	global_load_dword v241, v[124:125], off offset:128
	global_load_dword v242, v[124:125], off offset:192
	global_load_dword v243, v[124:125], off offset:512
	global_load_dword v244, v[124:125], off offset:576
	global_load_dword v245, v[124:125], off offset:640
	global_load_dword v246, v[124:125], off offset:704
	global_load_dwordx4 v[134:137], v[122:123], off
	global_load_dwordx4 v[130:133], v[122:123], off offset:16
	global_load_dwordx4 v[126:129], v[122:123], off offset:512
	s_nop 0
	global_load_dwordx4 v[122:125], v[122:123], off offset:528
	v_cvt_f32_i32_e32 v142, v142
	v_cvt_f32_i32_e32 v145, v145
	v_cvt_f32_i32_e32 v144, v144
	v_cvt_f32_i32_e32 v139, v139
	v_cvt_f32_i32_e32 v138, v138
	v_cvt_f32_i32_e32 v141, v141
	v_cvt_f32_i32_e32 v140, v140
	v_cvt_f32_i32_e32 v119, v119
	v_cvt_f32_i32_e32 v118, v118
	v_cvt_f32_i32_e32 v121, v121
	v_cvt_f32_i32_e32 v120, v120
	v_cvt_f32_i32_e32 v115, v115
	v_cvt_f32_i32_e32 v114, v114
	v_cvt_f32_i32_e32 v117, v117
	v_cvt_f32_i32_e32 v116, v116
	v_add_u32_e32 v154, 16, v164
	v_lshl_add_u64 v[176:177], v[154:155], 2, s[8:9]
	v_cvt_f32_i32_e32 v111, v111
	v_cvt_f32_i32_e32 v110, v110
	v_cvt_f32_i32_e32 v113, v113
	v_cvt_f32_i32_e32 v112, v112
	v_cvt_f32_i32_e32 v107, v107
	v_cvt_f32_i32_e32 v106, v106
	v_cvt_f32_i32_e32 v109, v109
	v_cvt_f32_i32_e32 v108, v108
	v_cvt_f32_i32_e32 v103, v103
	v_cvt_f32_i32_e32 v102, v102
	v_cvt_f32_i32_e32 v105, v105
	v_cvt_f32_i32_e32 v104, v104
	v_cvt_f32_i32_e32 v99, v99
	v_cvt_f32_i32_e32 v98, v98
	v_cvt_f32_i32_e32 v101, v101
	v_cvt_f32_i32_e32 v100, v100
	v_add_u32_e32 v165, 0x20000, v172
	v_add_u32_e32 v154, 32, v164
	v_cvt_f32_i32_e32 v95, v95
	v_cvt_f32_i32_e32 v94, v94
	v_cvt_f32_i32_e32 v97, v97
	v_cvt_f32_i32_e32 v96, v96
	v_cvt_f32_i32_e32 v91, v91
	v_cvt_f32_i32_e32 v90, v90
	v_cvt_f32_i32_e32 v93, v93
	v_cvt_f32_i32_e32 v92, v92
	v_cvt_f32_i32_e32 v87, v87
	v_cvt_f32_i32_e32 v86, v86
	v_cvt_f32_i32_e32 v89, v89
	v_cvt_f32_i32_e32 v88, v88
	v_cvt_f32_i32_e32 v83, v83
	v_cvt_f32_i32_e32 v82, v82
	v_cvt_f32_i32_e32 v85, v85
	v_cvt_f32_i32_e32 v84, v84
	v_cvt_f32_i32_e32 v79, v79
	v_cvt_f32_i32_e32 v78, v78
	v_cvt_f32_i32_e32 v81, v81
	v_cvt_f32_i32_e32 v80, v80
	v_cvt_f32_i32_e32 v75, v75
	v_cvt_f32_i32_e32 v74, v74
	v_cvt_f32_i32_e32 v77, v77
	v_cvt_f32_i32_e32 v76, v76
	v_cvt_f32_i32_e32 v71, v71
	v_cvt_f32_i32_e32 v70, v70
	v_cvt_f32_i32_e32 v73, v73
	v_cvt_f32_i32_e32 v72, v72
	v_cvt_f32_i32_e32 v67, v67
	v_cvt_f32_i32_e32 v66, v66
	v_cvt_f32_i32_e32 v69, v69
	v_cvt_f32_i32_e32 v68, v68
	v_cvt_f32_i32_e32 v63, v63
	v_cvt_f32_i32_e32 v62, v62
	v_cvt_f32_i32_e32 v65, v65
	v_cvt_f32_i32_e32 v64, v64
	v_cvt_f32_i32_e32 v59, v59
	v_cvt_f32_i32_e32 v58, v58
	v_cvt_f32_i32_e32 v61, v61
	v_cvt_f32_i32_e32 v60, v60
	v_cvt_f32_i32_e32 v55, v55
	s_waitcnt vmcnt(0)
	v_pk_mul_f32 v[178:179], v[134:135], v[174:175] op_sel_hi:[1,0]
	v_pk_mul_f32 v[180:181], v[136:137], v[174:175] op_sel_hi:[1,0]
	v_pk_mul_f32 v[182:183], v[130:131], v[174:175] op_sel_hi:[1,0]
	v_pk_mul_f32 v[184:185], v[132:133], v[174:175] op_sel_hi:[1,0]
	v_pk_mul_f32 v[186:187], v[126:127], v[174:175] op_sel_hi:[1,0]
	v_pk_mul_f32 v[188:189], v[128:129], v[174:175] op_sel_hi:[1,0]
	v_pk_mul_f32 v[190:191], v[122:123], v[174:175] op_sel_hi:[1,0]
	v_pk_mul_f32 v[174:175], v[124:125], v[174:175] op_sel_hi:[1,0]
	v_pk_mul_f32 v[142:143], v[178:179], v[142:143]
	v_pk_mul_f32 v[144:145], v[180:181], v[144:145]
	v_pk_mul_f32 v[138:139], v[182:183], v[138:139]
	v_pk_mul_f32 v[140:141], v[184:185], v[140:141]
	v_pk_mul_f32 v[118:119], v[186:187], v[118:119]
	v_pk_mul_f32 v[120:121], v[188:189], v[120:121]
	v_pk_mul_f32 v[178:179], v[190:191], v[114:115]
	v_pk_mul_f32 v[174:175], v[174:175], v[116:117]
	v_cvt_pk_f16_f32 v114, v142, v143
	v_cvt_pk_f16_f32 v115, v144, v145
	v_cvt_pk_f16_f32 v116, v138, v139
	v_cvt_pk_f16_f32 v117, v140, v141
	v_cvt_pk_f16_f32 v118, v118, v119
	v_cvt_pk_f16_f32 v119, v120, v121
	v_cvt_pk_f16_f32 v120, v178, v179
	v_cvt_pk_f16_f32 v121, v174, v175
	global_store_dwordx4 v172, v[114:117], s[12:13]
	global_store_dwordx4 v172, v[118:121], s[12:13] offset:256
	s_nop 0
	v_mov_b32_e32 v114, v240
	v_lshl_add_u64 v[116:117], v[154:155], 2, s[8:9]
	v_add_u32_e32 v154, 48, v164
	v_cvt_f32_i32_e32 v54, v54
	v_cvt_f32_i32_e32 v57, v57
	v_cvt_f32_i32_e32 v56, v56
	v_cvt_f32_i32_e32 v51, v51
	v_cvt_f32_i32_e32 v50, v50
	v_cvt_f32_i32_e32 v53, v53
	v_cvt_f32_i32_e32 v52, v52
	v_cvt_f32_i32_e32 v47, v47
	v_cvt_f32_i32_e32 v46, v46
	v_cvt_f32_i32_e32 v49, v49
	v_cvt_f32_i32_e32 v48, v48
	v_cvt_f32_i32_e32 v43, v43
	v_cvt_f32_i32_e32 v42, v42
	v_cvt_f32_i32_e32 v45, v45
	v_cvt_f32_i32_e32 v44, v44
	v_cvt_f32_i32_e32 v39, v39
	v_cvt_f32_i32_e32 v38, v38
	v_cvt_f32_i32_e32 v41, v41
	v_cvt_f32_i32_e32 v40, v40
	v_cvt_f32_i32_e32 v35, v35
	v_cvt_f32_i32_e32 v34, v34
	v_cvt_f32_i32_e32 v37, v37
	v_cvt_f32_i32_e32 v36, v36
	v_cvt_f32_i32_e32 v31, v31
	v_cvt_f32_i32_e32 v30, v30
	v_cvt_f32_i32_e32 v33, v33
	v_cvt_f32_i32_e32 v32, v32
	v_cvt_f32_i32_e32 v27, v27
	v_cvt_f32_i32_e32 v26, v26
	v_cvt_f32_i32_e32 v29, v29
	v_cvt_f32_i32_e32 v28, v28
	v_cvt_f32_i32_e32 v23, v23
	v_cvt_f32_i32_e32 v22, v22
	v_cvt_f32_i32_e32 v25, v25
	v_cvt_f32_i32_e32 v24, v24
	v_cvt_f32_i32_e32 v19, v19
	v_cvt_f32_i32_e32 v18, v18
	v_cvt_f32_i32_e32 v21, v21
	v_cvt_f32_i32_e32 v20, v20
	v_cvt_f32_i32_e32 v15, v15
	v_cvt_f32_i32_e32 v14, v14
	v_cvt_f32_i32_e32 v17, v17
	v_cvt_f32_i32_e32 v16, v16
	v_cvt_f32_i32_e32 v11, v11
	v_cvt_f32_i32_e32 v10, v10
	v_cvt_f32_i32_e32 v13, v13
	v_cvt_f32_i32_e32 v12, v12
	v_cvt_f32_i32_e32 v7, v7
	v_cvt_f32_i32_e32 v6, v6
	v_cvt_f32_i32_e32 v9, v9
	v_cvt_f32_i32_e32 v8, v8
	v_cvt_f32_i32_e32 v3, v3
	v_cvt_f32_i32_e32 v2, v2
	v_cvt_f32_i32_e32 v5, v5
	v_cvt_f32_i32_e32 v4, v4
	s_and_b64 vcc, exec, s[2:3]
	s_mov_b64 s[2:3], -1
	v_pk_mul_f32 v[118:119], v[134:135], v[114:115] op_sel_hi:[1,0]
	v_pk_mul_f32 v[120:121], v[136:137], v[114:115] op_sel_hi:[1,0]
	v_pk_mul_f32 v[138:139], v[130:131], v[114:115] op_sel_hi:[1,0]
	v_pk_mul_f32 v[140:141], v[132:133], v[114:115] op_sel_hi:[1,0]
	v_pk_mul_f32 v[142:143], v[126:127], v[114:115] op_sel_hi:[1,0]
	v_pk_mul_f32 v[144:145], v[128:129], v[114:115] op_sel_hi:[1,0]
	v_pk_mul_f32 v[174:175], v[122:123], v[114:115] op_sel_hi:[1,0]
	v_pk_mul_f32 v[114:115], v[124:125], v[114:115] op_sel_hi:[1,0]
	v_pk_mul_f32 v[110:111], v[118:119], v[110:111]
	v_pk_mul_f32 v[112:113], v[120:121], v[112:113]
	v_pk_mul_f32 v[106:107], v[138:139], v[106:107]
	v_pk_mul_f32 v[108:109], v[140:141], v[108:109]
	v_pk_mul_f32 v[102:103], v[142:143], v[102:103]
	v_pk_mul_f32 v[104:105], v[144:145], v[104:105]
	v_pk_mul_f32 v[118:119], v[174:175], v[98:99]
	v_pk_mul_f32 v[114:115], v[114:115], v[100:101]
	v_cvt_pk_f16_f32 v98, v110, v111
	v_cvt_pk_f16_f32 v99, v112, v113
	v_cvt_pk_f16_f32 v100, v106, v107
	v_cvt_pk_f16_f32 v101, v108, v109
	v_cvt_pk_f16_f32 v102, v102, v103
	v_cvt_pk_f16_f32 v103, v104, v105
	v_cvt_pk_f16_f32 v104, v118, v119
	v_cvt_pk_f16_f32 v105, v114, v115
	global_store_dwordx4 v165, v[98:101], s[12:13]
	global_store_dwordx4 v165, v[102:105], s[12:13] offset:256
	s_nop 0
	v_mov_b32_e32 v98, v241
	v_add_u32_e32 v116, 0x40000, v172
	v_lshl_add_u64 v[100:101], v[154:155], 2, s[8:9]
	v_add_u32_e32 v154, 0x80, v164
	v_pk_mul_f32 v[102:103], v[134:135], v[98:99] op_sel_hi:[1,0]
	v_pk_mul_f32 v[104:105], v[136:137], v[98:99] op_sel_hi:[1,0]
	v_pk_mul_f32 v[106:107], v[130:131], v[98:99] op_sel_hi:[1,0]
	v_pk_mul_f32 v[108:109], v[132:133], v[98:99] op_sel_hi:[1,0]
	v_pk_mul_f32 v[110:111], v[126:127], v[98:99] op_sel_hi:[1,0]
	v_pk_mul_f32 v[112:113], v[128:129], v[98:99] op_sel_hi:[1,0]
	v_pk_mul_f32 v[114:115], v[122:123], v[98:99] op_sel_hi:[1,0]
	v_pk_mul_f32 v[98:99], v[124:125], v[98:99] op_sel_hi:[1,0]
	v_pk_mul_f32 v[94:95], v[102:103], v[94:95]
	v_pk_mul_f32 v[96:97], v[104:105], v[96:97]
	v_pk_mul_f32 v[90:91], v[106:107], v[90:91]
	v_pk_mul_f32 v[92:93], v[108:109], v[92:93]
	v_pk_mul_f32 v[86:87], v[110:111], v[86:87]
	v_pk_mul_f32 v[88:89], v[112:113], v[88:89]
	v_pk_mul_f32 v[102:103], v[114:115], v[82:83]
	v_pk_mul_f32 v[98:99], v[98:99], v[84:85]
	v_cvt_pk_f16_f32 v82, v94, v95
	v_cvt_pk_f16_f32 v83, v96, v97
	v_cvt_pk_f16_f32 v84, v90, v91
	v_cvt_pk_f16_f32 v85, v92, v93
	v_cvt_pk_f16_f32 v86, v86, v87
	v_cvt_pk_f16_f32 v87, v88, v89
	v_cvt_pk_f16_f32 v88, v102, v103
	v_cvt_pk_f16_f32 v89, v98, v99
	global_store_dwordx4 v116, v[82:85], s[12:13]
	global_store_dwordx4 v116, v[86:89], s[12:13] offset:256
	s_nop 0
	v_mov_b32_e32 v82, v242
	v_add_u32_e32 v100, 0x60000, v172
	v_lshl_add_u64 v[84:85], v[154:155], 2, s[8:9]
	v_add_u32_e32 v154, 0x90, v164
	v_pk_mul_f32 v[86:87], v[134:135], v[82:83] op_sel_hi:[1,0]
	v_pk_mul_f32 v[88:89], v[136:137], v[82:83] op_sel_hi:[1,0]
	v_pk_mul_f32 v[90:91], v[130:131], v[82:83] op_sel_hi:[1,0]
	v_pk_mul_f32 v[92:93], v[132:133], v[82:83] op_sel_hi:[1,0]
	v_pk_mul_f32 v[94:95], v[126:127], v[82:83] op_sel_hi:[1,0]
	v_pk_mul_f32 v[96:97], v[128:129], v[82:83] op_sel_hi:[1,0]
	v_pk_mul_f32 v[98:99], v[122:123], v[82:83] op_sel_hi:[1,0]
	v_pk_mul_f32 v[82:83], v[124:125], v[82:83] op_sel_hi:[1,0]
	v_pk_mul_f32 v[78:79], v[86:87], v[78:79]
	v_pk_mul_f32 v[80:81], v[88:89], v[80:81]
	v_pk_mul_f32 v[74:75], v[90:91], v[74:75]
	v_pk_mul_f32 v[76:77], v[92:93], v[76:77]
	v_pk_mul_f32 v[70:71], v[94:95], v[70:71]
	v_pk_mul_f32 v[72:73], v[96:97], v[72:73]
	v_pk_mul_f32 v[86:87], v[98:99], v[66:67]
	v_pk_mul_f32 v[82:83], v[82:83], v[68:69]
	v_cvt_pk_f16_f32 v66, v78, v79
	v_cvt_pk_f16_f32 v67, v80, v81
	v_cvt_pk_f16_f32 v68, v74, v75
	v_cvt_pk_f16_f32 v69, v76, v77
	v_cvt_pk_f16_f32 v70, v70, v71
	v_cvt_pk_f16_f32 v71, v72, v73
	v_cvt_pk_f16_f32 v72, v86, v87
	v_cvt_pk_f16_f32 v73, v82, v83
	global_store_dwordx4 v100, v[66:69], s[12:13]
	global_store_dwordx4 v100, v[70:73], s[12:13] offset:256
	s_nop 0
	v_mov_b32_e32 v66, v243
	v_add_u32_e32 v84, 0x100000, v172
	v_lshl_add_u64 v[68:69], v[154:155], 2, s[8:9]
	v_add_u32_e32 v154, 0xa0, v164
	v_pk_mul_f32 v[70:71], v[134:135], v[66:67] op_sel_hi:[1,0]
	v_pk_mul_f32 v[72:73], v[136:137], v[66:67] op_sel_hi:[1,0]
	v_pk_mul_f32 v[74:75], v[130:131], v[66:67] op_sel_hi:[1,0]
	v_pk_mul_f32 v[76:77], v[132:133], v[66:67] op_sel_hi:[1,0]
	v_pk_mul_f32 v[78:79], v[126:127], v[66:67] op_sel_hi:[1,0]
	v_pk_mul_f32 v[80:81], v[128:129], v[66:67] op_sel_hi:[1,0]
	v_pk_mul_f32 v[82:83], v[122:123], v[66:67] op_sel_hi:[1,0]
	v_pk_mul_f32 v[66:67], v[124:125], v[66:67] op_sel_hi:[1,0]
	v_pk_mul_f32 v[62:63], v[70:71], v[62:63]
	v_pk_mul_f32 v[64:65], v[72:73], v[64:65]
	v_pk_mul_f32 v[58:59], v[74:75], v[58:59]
	v_pk_mul_f32 v[60:61], v[76:77], v[60:61]
	v_pk_mul_f32 v[54:55], v[78:79], v[54:55]
	v_pk_mul_f32 v[56:57], v[80:81], v[56:57]
	v_pk_mul_f32 v[70:71], v[82:83], v[50:51]
	v_pk_mul_f32 v[66:67], v[66:67], v[52:53]
	v_cvt_pk_f16_f32 v50, v62, v63
	v_cvt_pk_f16_f32 v51, v64, v65
	v_cvt_pk_f16_f32 v52, v58, v59
	v_cvt_pk_f16_f32 v53, v60, v61
	v_cvt_pk_f16_f32 v54, v54, v55
	v_cvt_pk_f16_f32 v55, v56, v57
	v_cvt_pk_f16_f32 v56, v70, v71
	v_cvt_pk_f16_f32 v57, v66, v67
	global_store_dwordx4 v84, v[50:53], s[12:13]
	global_store_dwordx4 v84, v[54:57], s[12:13] offset:256
	s_nop 0
	v_mov_b32_e32 v50, v244
	v_add_u32_e32 v68, 0x120000, v172
	v_lshl_add_u64 v[52:53], v[154:155], 2, s[8:9]
	v_add_u32_e32 v154, 0xb0, v164
	v_pk_mul_f32 v[54:55], v[134:135], v[50:51] op_sel_hi:[1,0]
	v_pk_mul_f32 v[56:57], v[136:137], v[50:51] op_sel_hi:[1,0]
	v_pk_mul_f32 v[58:59], v[130:131], v[50:51] op_sel_hi:[1,0]
	v_pk_mul_f32 v[60:61], v[132:133], v[50:51] op_sel_hi:[1,0]
	v_pk_mul_f32 v[62:63], v[126:127], v[50:51] op_sel_hi:[1,0]
	v_pk_mul_f32 v[64:65], v[128:129], v[50:51] op_sel_hi:[1,0]
	v_pk_mul_f32 v[66:67], v[122:123], v[50:51] op_sel_hi:[1,0]
	v_pk_mul_f32 v[50:51], v[124:125], v[50:51] op_sel_hi:[1,0]
	v_pk_mul_f32 v[46:47], v[54:55], v[46:47]
	v_pk_mul_f32 v[48:49], v[56:57], v[48:49]
	v_pk_mul_f32 v[42:43], v[58:59], v[42:43]
	v_pk_mul_f32 v[44:45], v[60:61], v[44:45]
	v_pk_mul_f32 v[38:39], v[62:63], v[38:39]
	v_pk_mul_f32 v[40:41], v[64:65], v[40:41]
	v_pk_mul_f32 v[54:55], v[66:67], v[34:35]
	v_pk_mul_f32 v[50:51], v[50:51], v[36:37]
	v_cvt_pk_f16_f32 v34, v46, v47
	v_cvt_pk_f16_f32 v35, v48, v49
	v_cvt_pk_f16_f32 v36, v42, v43
	v_cvt_pk_f16_f32 v37, v44, v45
	v_cvt_pk_f16_f32 v38, v38, v39
	v_cvt_pk_f16_f32 v39, v40, v41
	v_cvt_pk_f16_f32 v40, v54, v55
	v_cvt_pk_f16_f32 v41, v50, v51
	global_store_dwordx4 v68, v[34:37], s[12:13]
	global_store_dwordx4 v68, v[38:41], s[12:13] offset:256
	s_nop 0
	v_mov_b32_e32 v34, v245
	v_add_u32_e32 v52, 0x140000, v172
	v_lshl_add_u64 v[36:37], v[154:155], 2, s[8:9]
	v_pk_mul_f32 v[38:39], v[134:135], v[34:35] op_sel_hi:[1,0]
	v_pk_mul_f32 v[40:41], v[136:137], v[34:35] op_sel_hi:[1,0]
	v_pk_mul_f32 v[42:43], v[130:131], v[34:35] op_sel_hi:[1,0]
	v_pk_mul_f32 v[44:45], v[132:133], v[34:35] op_sel_hi:[1,0]
	v_pk_mul_f32 v[46:47], v[126:127], v[34:35] op_sel_hi:[1,0]
	v_pk_mul_f32 v[48:49], v[128:129], v[34:35] op_sel_hi:[1,0]
	v_pk_mul_f32 v[50:51], v[122:123], v[34:35] op_sel_hi:[1,0]
	v_pk_mul_f32 v[34:35], v[124:125], v[34:35] op_sel_hi:[1,0]
	v_pk_mul_f32 v[30:31], v[38:39], v[30:31]
	v_pk_mul_f32 v[32:33], v[40:41], v[32:33]
	v_pk_mul_f32 v[26:27], v[42:43], v[26:27]
	v_pk_mul_f32 v[28:29], v[44:45], v[28:29]
	v_pk_mul_f32 v[22:23], v[46:47], v[22:23]
	v_pk_mul_f32 v[24:25], v[48:49], v[24:25]
	v_pk_mul_f32 v[38:39], v[50:51], v[18:19]
	v_pk_mul_f32 v[34:35], v[34:35], v[20:21]
	v_cvt_pk_f16_f32 v18, v30, v31
	v_cvt_pk_f16_f32 v19, v32, v33
	v_cvt_pk_f16_f32 v20, v26, v27
	v_cvt_pk_f16_f32 v21, v28, v29
	v_cvt_pk_f16_f32 v22, v22, v23
	v_cvt_pk_f16_f32 v23, v24, v25
	v_cvt_pk_f16_f32 v24, v38, v39
	v_cvt_pk_f16_f32 v25, v34, v35
	global_store_dwordx4 v52, v[18:21], s[12:13]
	global_store_dwordx4 v52, v[22:25], s[12:13] offset:256
	s_nop 0
	v_mov_b32_e32 v18, v246
	v_add_u32_e32 v34, 0x160000, v172
	v_pk_mul_f32 v[20:21], v[134:135], v[18:19] op_sel_hi:[1,0]
	v_pk_mul_f32 v[22:23], v[136:137], v[18:19] op_sel_hi:[1,0]
	v_pk_mul_f32 v[24:25], v[130:131], v[18:19] op_sel_hi:[1,0]
	v_pk_mul_f32 v[26:27], v[132:133], v[18:19] op_sel_hi:[1,0]
	v_pk_mul_f32 v[28:29], v[126:127], v[18:19] op_sel_hi:[1,0]
	v_pk_mul_f32 v[30:31], v[128:129], v[18:19] op_sel_hi:[1,0]
	v_pk_mul_f32 v[32:33], v[122:123], v[18:19] op_sel_hi:[1,0]
	v_pk_mul_f32 v[18:19], v[124:125], v[18:19] op_sel_hi:[1,0]
	v_pk_mul_f32 v[14:15], v[20:21], v[14:15]
	v_pk_mul_f32 v[16:17], v[22:23], v[16:17]
	v_pk_mul_f32 v[10:11], v[24:25], v[10:11]
	v_pk_mul_f32 v[12:13], v[26:27], v[12:13]
	v_pk_mul_f32 v[6:7], v[28:29], v[6:7]
	v_pk_mul_f32 v[8:9], v[30:31], v[8:9]
	v_pk_mul_f32 v[20:21], v[32:33], v[2:3]
	v_pk_mul_f32 v[18:19], v[18:19], v[4:5]
	v_cvt_pk_f16_f32 v2, v14, v15
	v_cvt_pk_f16_f32 v3, v16, v17
	v_cvt_pk_f16_f32 v4, v10, v11
	v_cvt_pk_f16_f32 v5, v12, v13
	v_cvt_pk_f16_f32 v6, v6, v7
	v_cvt_pk_f16_f32 v7, v8, v9
	v_cvt_pk_f16_f32 v8, v20, v21
	v_cvt_pk_f16_f32 v9, v18, v19
	global_store_dwordx4 v34, v[2:5], s[12:13]
	global_store_dwordx4 v34, v[6:9], s[12:13] offset:256
	s_cbranch_vccnz .LBB0_1887
	s_andn2_b64 vcc, exec, s[6:7]
	s_cbranch_vccnz .LBB0_1886
	s_barrier
	s_branch .LBB0_1886
